# mix GEMM epilogue: attention-gate words kept in registers from the mid hook (ai=0 re-read mid-hook into freed pairs) instead of 16 loads at epilogue start
# speedup vs baseline: 1.0042x; 1.0041x over previous
.Lmid1046:
	ds_read_b128 v[136:139], v175
	ds_read_b128 v[140:143], v175 offset:1024
	ds_read_b128 v[144:147], v175 offset:2048
	ds_read_b128 v[148:151], v175 offset:3072
	ds_read_b128 v[152:155], v176
	ds_read_b128 v[156:159], v176 offset:1024
	ds_read_b128 v[160:163], v176 offset:2048
	ds_read_b128 v[178:181], v176 offset:3072
	ds_read_b128 v[182:185], v174 offset:32768
	ds_read_b128 v[186:189], v174 offset:33792
	ds_read_b128 v[190:193], v174 offset:34816
	ds_read_b128 v[194:197], v174 offset:35840
	ds_read_b128 v[198:201], v174 offset:36864
	ds_read_b128 v[202:205], v174 offset:37888
	ds_read_b128 v[206:209], v174 offset:38912
	ds_read_b128 v[210:213], v174 offset:39936
	s_add_u32 s28, s25, 0x40100
	s_addc_u32 s29, s33, 0
	s_mov_b32 s25, m0
	s_mov_b32 m0, s85
	s_nop 2
	global_load_lds_dwordx4 v165, s[28:29]
	s_mov_b32 m0, s25
	s_nop 0
	s_mov_b32 s25, m0
	s_mov_b32 m0, s86
	s_nop 2
	global_load_lds_dwordx4 v167, s[28:29]
	s_mov_b32 m0, s25
	s_waitcnt vmcnt(8)
	s_waitcnt lgkmcnt(0)
	s_barrier
	s_setprio 1
	s_waitcnt lgkmcnt(7)
	v_mfma_f32_16x16x32_bf16 v[26:29], v[136:139], v[182:185], v[26:29]
	v_mfma_f32_16x16x32_bf16 v[30:33], v[144:147], v[182:185], v[30:33]
	s_waitcnt lgkmcnt(5)
	v_mfma_f32_16x16x32_bf16 v[50:53], v[136:139], v[190:193], v[50:53]
	v_mfma_f32_16x16x32_bf16 v[54:57], v[144:147], v[190:193], v[54:57]
	s_waitcnt lgkmcnt(3)
	v_mfma_f32_16x16x32_bf16 v[74:77], v[136:139], v[198:201], v[74:77]
	v_mfma_f32_16x16x32_bf16 v[78:81], v[144:147], v[198:201], v[78:81]
	s_waitcnt lgkmcnt(1)
	v_mfma_f32_16x16x32_bf16 v[94:97], v[136:139], v[206:209], v[94:97]
	v_mfma_f32_16x16x32_bf16 v[102:105], v[144:147], v[206:209], v[102:105]
	v_mfma_f32_16x16x32_bf16 v[26:29], v[140:143], v[186:189], v[26:29]
	v_mfma_f32_16x16x32_bf16 v[30:33], v[148:151], v[186:189], v[30:33]
	v_mfma_f32_16x16x32_bf16 v[50:53], v[140:143], v[194:197], v[50:53]
	v_mfma_f32_16x16x32_bf16 v[54:57], v[148:151], v[194:197], v[54:57]
	v_mfma_f32_16x16x32_bf16 v[74:77], v[140:143], v[202:205], v[74:77]
	v_mfma_f32_16x16x32_bf16 v[78:81], v[148:151], v[202:205], v[78:81]
	s_waitcnt lgkmcnt(0)
	v_mfma_f32_16x16x32_bf16 v[94:97], v[140:143], v[210:213], v[94:97]
	v_mfma_f32_16x16x32_bf16 v[102:105], v[148:151], v[210:213], v[102:105]
	s_setprio 0
	s_setprio 1
	v_mfma_f32_16x16x32_bf16 v[38:41], v[152:155], v[182:185], v[38:41]
	v_mfma_f32_16x16x32_bf16 v[42:45], v[160:163], v[182:185], v[42:45]
	v_mfma_f32_16x16x32_bf16 v[62:65], v[152:155], v[190:193], v[62:65]
	v_mfma_f32_16x16x32_bf16 v[66:69], v[160:163], v[190:193], v[66:69]
	v_mfma_f32_16x16x32_bf16 v[82:85], v[152:155], v[198:201], v[82:85]
	v_mfma_f32_16x16x32_bf16 v[90:93], v[160:163], v[198:201], v[90:93]
	v_mfma_f32_16x16x32_bf16 v[106:109], v[152:155], v[206:209], v[106:109]
	v_mfma_f32_16x16x32_bf16 v[114:117], v[160:163], v[206:209], v[114:117]
	v_mfma_f32_16x16x32_bf16 v[38:41], v[156:159], v[186:189], v[38:41]
	v_mfma_f32_16x16x32_bf16 v[42:45], v[178:181], v[186:189], v[42:45]
	v_mfma_f32_16x16x32_bf16 v[62:65], v[156:159], v[194:197], v[62:65]
	v_mfma_f32_16x16x32_bf16 v[66:69], v[178:181], v[194:197], v[66:69]
	v_mfma_f32_16x16x32_bf16 v[82:85], v[156:159], v[202:205], v[82:85]
	v_mfma_f32_16x16x32_bf16 v[90:93], v[178:181], v[202:205], v[90:93]
	v_mfma_f32_16x16x32_bf16 v[106:109], v[156:159], v[210:213], v[106:109]
	v_mfma_f32_16x16x32_bf16 v[114:117], v[178:181], v[210:213], v[114:117]
	s_setprio 0
	s_barrier
	ds_read_b128 v[182:185], v174 offset:49152
	ds_read_b128 v[186:189], v174 offset:50176
	ds_read_b128 v[190:193], v174 offset:51200
	ds_read_b128 v[194:197], v174 offset:52224
	ds_read_b128 v[198:201], v174 offset:53248
	ds_read_b128 v[202:205], v174 offset:54272
	ds_read_b128 v[206:209], v174 offset:55296
	ds_read_b128 v[210:213], v174 offset:56320
	s_add_u32 s28, s23, 0x180
	s_addc_u32 s29, s24, 0
	s_mov_b32 s25, m0
	s_mov_b32 m0, s92
	s_nop 2
	global_load_lds_dwordx4 v166, s[28:29]
	s_mov_b32 m0, s25
	s_nop 0
	s_mov_b32 s25, m0
	s_mov_b32 m0, s93
	s_nop 2
	global_load_lds_dwordx4 v168, s[28:29]
	s_mov_b32 m0, s25
	s_add_u32 s28, s23, 0x40180
	s_addc_u32 s29, s24, 0
	s_mov_b32 s23, m0
	s_mov_b32 m0, s96
	s_nop 2
	global_load_lds_dwordx4 v166, s[28:29]
	s_mov_b32 m0, s23
	s_nop 0
	s_mov_b32 s23, m0
	s_mov_b32 m0, s97
	s_nop 2
	global_load_lds_dwordx4 v168, s[28:29]
	s_mov_b32 m0, s23
	s_nop 0
	s_mov_b32 s23, m0
	s_mov_b32 m0, s94
	s_nop 2
	global_load_lds_dwordx4 v165, s[58:59]
	s_mov_b32 m0, s23
	s_nop 0
	s_mov_b32 s23, m0
	s_mov_b32 m0, s95
	s_nop 2
	global_load_lds_dwordx4 v167, s[58:59]
	s_mov_b32 m0, s23
	s_waitcnt vmcnt(8)
	s_waitcnt lgkmcnt(0)
	s_barrier
	s_setprio 1
	s_waitcnt lgkmcnt(7)
	v_mfma_f32_16x16x32_bf16 v[118:121], v[136:139], v[182:185], v[118:121]
	v_mfma_f32_16x16x32_bf16 v[126:129], v[144:147], v[182:185], v[126:129]
	s_waitcnt lgkmcnt(5)
	v_mfma_f32_16x16x32_bf16 v[98:101], v[136:139], v[190:193], v[98:101]
	v_mfma_f32_16x16x32_bf16 v[86:89], v[144:147], v[190:193], v[86:89]
	s_waitcnt lgkmcnt(3)
	v_mfma_f32_16x16x32_bf16 v[46:49], v[136:139], v[198:201], v[46:49]
	v_mfma_f32_16x16x32_bf16 v[34:37], v[144:147], v[198:201], v[34:37]
	s_waitcnt lgkmcnt(1)
	v_mfma_f32_16x16x32_bf16 v[14:17], v[136:139], v[206:209], v[14:17]
	v_mfma_f32_16x16x32_bf16 v[10:13], v[144:147], v[206:209], v[10:13]
	v_mfma_f32_16x16x32_bf16 v[118:121], v[140:143], v[186:189], v[118:121]
	v_mfma_f32_16x16x32_bf16 v[126:129], v[148:151], v[186:189], v[126:129]
	v_mfma_f32_16x16x32_bf16 v[98:101], v[140:143], v[194:197], v[98:101]
	v_mfma_f32_16x16x32_bf16 v[86:89], v[148:151], v[194:197], v[86:89]
	v_mfma_f32_16x16x32_bf16 v[46:49], v[140:143], v[202:205], v[46:49]
	v_mfma_f32_16x16x32_bf16 v[34:37], v[148:151], v[202:205], v[34:37]
	s_waitcnt lgkmcnt(0)
	v_mfma_f32_16x16x32_bf16 v[14:17], v[140:143], v[210:213], v[14:17]
	v_mfma_f32_16x16x32_bf16 v[10:13], v[148:151], v[210:213], v[10:13]
	s_setprio 0
	s_setprio 1
	v_mfma_f32_16x16x32_bf16 v[122:125], v[152:155], v[182:185], v[122:125]
	v_mfma_f32_16x16x32_bf16 v[110:113], v[160:163], v[182:185], v[110:113]
	v_mfma_f32_16x16x32_bf16 v[70:73], v[152:155], v[190:193], v[70:73]
	v_mfma_f32_16x16x32_bf16 v[58:61], v[160:163], v[190:193], v[58:61]
	v_mfma_f32_16x16x32_bf16 v[22:25], v[152:155], v[198:201], v[22:25]
	v_mfma_f32_16x16x32_bf16 v[18:21], v[160:163], v[198:201], v[18:21]
	v_mfma_f32_16x16x32_bf16 v[6:9], v[152:155], v[206:209], v[6:9]
	v_mfma_f32_16x16x32_bf16 v[2:5], v[160:163], v[206:209], v[2:5]
	v_mfma_f32_16x16x32_bf16 v[122:125], v[156:159], v[186:189], v[122:125]
	v_mfma_f32_16x16x32_bf16 v[110:113], v[178:181], v[186:189], v[110:113]
	v_mfma_f32_16x16x32_bf16 v[70:73], v[156:159], v[194:197], v[70:73]
	v_mfma_f32_16x16x32_bf16 v[58:61], v[178:181], v[194:197], v[58:61]
	v_mfma_f32_16x16x32_bf16 v[22:25], v[156:159], v[202:205], v[22:25]
	v_mfma_f32_16x16x32_bf16 v[18:21], v[178:181], v[202:205], v[18:21]
	v_mfma_f32_16x16x32_bf16 v[6:9], v[156:159], v[210:213], v[6:9]
	v_mfma_f32_16x16x32_bf16 v[2:5], v[178:181], v[210:213], v[2:5]
	s_setprio 0
	s_barrier
	s_add_i32 s3, s3, 2
	s_add_u32 s56, s56, 0x100
	s_addc_u32 s57, s57, 0
	s_cmp_gt_u32 s3, 5
	s_cbranch_scc0 .LBB0_1046
	s_ashr_i32 s55, s54, 31
	s_lshl_b64 s[24:25], s[54:55], 19
	s_add_u32 s56, s69, s24
	s_addc_u32 s57, s76, s25
	s_ashr_i32 s23, s22, 31
	s_lshl_b64 s[24:25], s[22:23], 19
	s_add_u32 s58, s77, s24
	s_addc_u32 s59, s78, s25
	s_lshl_b32 s3, s60, 18
	s_lshl_b32 s23, s2, 8
	s_lshl_b32 s32, s2, 16
	s_add_i32 s2, s32, s3
	v_lshrrev_b32_e32 v214, 6, v0
	v_lshlrev_b32_e32 v214, 13, v214
	v_and_b32_e32 v215, 63, v0
	v_lshl_add_u32 v214, v215, 3, v214
	v_add_u32_e32 v134, s2, v214
	global_load_dwordx2 v[162:163], v134, s[14:15]
	global_load_dwordx2 v[178:179], v134, s[16:17]
	v_or_b32_e32 v136, 0x200, v134
	v_add_u32_e32 v137, 0x400, v134
	v_add_u32_e32 v138, 0x600, v134
	v_add_u32_e32 v139, 0x800, v134
	v_add_u32_e32 v140, 0xa00, v134
	v_add_u32_e32 v141, 0xc00, v134
	v_add_u32_e32 v161, 0xe00, v134
	global_load_dwordx2 v[180:181], v136, s[14:15]
	global_load_dwordx2 v[182:183], v136, s[16:17]
	global_load_dwordx2 v[158:159], v137, s[14:15]
	global_load_dwordx2 v[156:157], v137, s[16:17]
	global_load_dwordx2 v[154:155], v138, s[14:15]
	global_load_dwordx2 v[152:153], v138, s[16:17]
	global_load_dwordx2 v[150:151], v139, s[14:15]
	global_load_dwordx2 v[148:149], v139, s[16:17]
	global_load_dwordx2 v[146:147], v140, s[14:15]
	global_load_dwordx2 v[144:145], v140, s[16:17]
	global_load_dwordx2 v[142:143], v141, s[14:15]
	s_nop 0
	global_load_dwordx2 v[140:141], v141, s[16:17]
	s_nop 0
	global_load_dwordx2 v[138:139], v161, s[14:15]
	global_load_dwordx2 v[136:137], v161, s[16:17]
	v_add_u32_e32 v160, 0x1000, v134
	global_load_dwordx2 v[220:221], v160, s[14:15]
	global_load_dwordx2 v[222:223], v160, s[16:17]
	v_add_u32_e32 v219, 0x1200, v134
	v_add_u32_e32 v215, 0x1400, v134
	v_add_u32_e32 v216, 0x1600, v134
	v_add_u32_e32 v217, 0x1800, v134
	global_load_dwordx2 v[224:225], v219, s[14:15]
	global_load_dwordx2 v[226:227], v219, s[16:17]
	global_load_dwordx2 v[228:229], v215, s[14:15]
	global_load_dwordx2 v[230:231], v215, s[16:17]
	global_load_dwordx2 v[232:233], v216, s[14:15]
	global_load_dwordx2 v[234:235], v216, s[16:17]
	global_load_dwordx2 v[236:237], v217, s[14:15]
	global_load_dwordx2 v[238:239], v217, s[16:17]
	v_add_u32_e32 v219, 0x1a00, v134
	v_add_u32_e32 v215, 0x1c00, v134
	v_add_u32_e32 v216, 0x1e00, v134
	global_load_dwordx2 v[240:241], v219, s[14:15]
	global_load_dwordx2 v[242:243], v219, s[16:17]
	global_load_dwordx2 v[244:245], v215, s[14:15]
	global_load_dwordx2 v[246:247], v215, s[16:17]
	global_load_dwordx2 v[248:249], v216, s[14:15]
	global_load_dwordx2 v[250:251], v216, s[16:17]
	s_and_b64 s[2:3], s[4:5], exec
	s_cselect_b32 s2, s57, s65
	s_cselect_b32 s3, s56, s64
	s_cselect_b32 s24, s59, s63
	s_cselect_b32 s25, s58, s62
	s_add_u32 s28, s64, 0x500
	s_addc_u32 s29, s65, 0
	s_add_u32 s30, s62, 0x500
	s_addc_u32 s31, s63, 0
	s_mov_b32 s33, 6
	s_waitcnt vmcnt(31)
	v_cvt_pk_f32_fp8_e32 v[184:185], v162
	s_waitcnt vmcnt(30)
	v_cvt_pk_f32_fp8_e32 v[190:191], v178
	v_cvt_pk_f32_fp8_e32 v[188:189], v163
	v_cvt_pk_f32_fp8_sdwa v[192:193], v178 src0_sel:WORD_1
	v_cvt_pk_f32_fp8_e32 v[194:195], v179
	v_max_f32_e32 v161, v190, v190
	v_max_f32_e32 v190, v191, v191
	v_med3_f32 v161, v161, s35, v177
	v_med3_f32 v184, v184, s35, v177
	v_max_f32_e32 v191, v192, v192
	v_max_f32_e32 v192, v193, v193
	v_max_f32_e32 v193, v194, v194
	v_max_f32_e32 v194, v195, v195
	v_med3_f32 v190, v190, s35, v177
	v_med3_f32 v185, v185, s35, v177
	v_med3_f32 v188, v188, s35, v177
	v_mul_f32_e32 v161, 0xbfb8aa3b, v161
	v_mul_f32_e32 v195, 0xbfb8aa3b, v184
	v_cvt_pk_f32_fp8_sdwa v[186:187], v162 src0_sel:WORD_1
	v_cvt_pk_f32_fp8_sdwa v[162:163], v163 src0_sel:WORD_1
	v_med3_f32 v194, v194, s35, v177
	v_med3_f32 v189, v189, s35, v177
	v_mul_f32_e32 v190, 0xbfb8aa3b, v190
	v_mul_f32_e32 v196, 0xbfb8aa3b, v185
	v_mul_f32_e32 v199, 0xbfb8aa3b, v188
	v_exp_f32_e32 v184, v161
	v_exp_f32_e32 v161, v195
	v_mul_f32_e32 v200, 0xbfb8aa3b, v194
	v_mul_f32_e32 v189, 0xbfb8aa3b, v189
	v_exp_f32_e32 v185, v190
	v_exp_f32_e32 v190, v196
	v_exp_f32_e32 v194, v199
	v_exp_f32_e32 v195, v189
	v_cvt_pk_f32_fp8_sdwa v[178:179], v179 src0_sel:WORD_1
	v_add_f32_e32 v161, 1.0, v161
	v_add_f32_e32 v189, 1.0, v190
	v_rcp_f32_e32 v190, v161
	v_add_f32_e32 v161, 1.0, v194
	v_med3_f32 v162, v162, s35, v177
	v_rcp_f32_e32 v194, v161
	v_add_f32_e32 v161, 1.0, v195
	v_mul_f32_e32 v162, 0xbfb8aa3b, v162
	v_rcp_f32_e32 v195, v161
	v_max_f32_e32 v161, v178, v178
	v_exp_f32_e32 v178, v162
	v_med3_f32 v161, v161, s35, v177
	v_med3_f32 v163, v163, s35, v177
	v_mul_f32_e32 v161, 0xbfb8aa3b, v161
	v_mul_f32_e32 v163, 0xbfb8aa3b, v163
	v_exp_f32_e32 v162, v161
	v_add_f32_e32 v161, 1.0, v178
	v_max_f32_e32 v178, v179, v179
	v_exp_f32_e32 v179, v163
	v_med3_f32 v191, v191, s35, v177
	v_med3_f32 v186, v186, s35, v177
	v_med3_f32 v192, v192, s35, v177
	v_med3_f32 v187, v187, s35, v177
	v_mul_f32_e32 v191, 0xbfb8aa3b, v191
	v_mul_f32_e32 v197, 0xbfb8aa3b, v186
	v_mul_f32_e32 v192, 0xbfb8aa3b, v192
	v_mul_f32_e32 v198, 0xbfb8aa3b, v187
	v_med3_f32 v178, v178, s35, v177
	v_exp_f32_e32 v186, v191
	v_exp_f32_e32 v191, v197
	v_exp_f32_e32 v187, v192
	v_exp_f32_e32 v192, v198
	v_mul_f32_e32 v163, 0xbfb8aa3b, v178
	v_exp_f32_e32 v163, v163
	v_rcp_f32_e32 v178, v161
	v_add_f32_e32 v161, 1.0, v179
	v_med3_f32 v193, v193, s35, v177
	v_rcp_f32_e32 v179, v161
	v_mul_f32_e32 v193, 0xbfb8aa3b, v193
	v_exp_f32_e32 v188, v193
	v_add_f32_e32 v193, 1.0, v191
	v_add_f32_e32 v196, 1.0, v192
	v_rcp_f32_e32 v192, v193
	v_rcp_f32_e32 v193, v196
	v_pk_add_f32 v[162:163], v[162:163], 1.0 op_sel_hi:[1,0]
	v_pk_add_f32 v[186:187], v[186:187], 1.0 op_sel_hi:[1,0]
	v_pk_mul_f32 v[162:163], v[178:179], v[162:163]
	v_pk_mul_f32 v[186:187], v[192:193], v[186:187]
	v_pk_mul_f32 v[32:33], v[32:33], v[162:163]
	s_waitcnt vmcnt(29)
	v_cvt_pk_f32_fp8_e32 v[162:163], v180
	v_pk_mul_f32 v[28:29], v[28:29], v[186:187]
	s_waitcnt vmcnt(28)
	v_cvt_pk_f32_fp8_e32 v[186:187], v182
	v_rcp_f32_e32 v191, v189
	v_med3_f32 v162, v162, s35, v177
	v_mul_f32_e32 v162, 0xbfb8aa3b, v162
	v_max_f32_e32 v161, v186, v186
	v_exp_f32_e32 v186, v162
	v_exp_f32_e32 v189, v200
	v_med3_f32 v161, v161, s35, v177
	v_cvt_pk_f32_fp8_sdwa v[178:179], v180 src0_sel:WORD_1
	v_mul_f32_e32 v161, 0xbfb8aa3b, v161
	v_med3_f32 v163, v163, s35, v177
	v_pk_add_f32 v[184:185], v[184:185], 1.0 op_sel_hi:[1,0]
	v_exp_f32_e32 v162, v161
	v_add_f32_e32 v161, 1.0, v186
	v_mul_f32_e32 v163, 0xbfb8aa3b, v163
	v_pk_mul_f32 v[184:185], v[190:191], v[184:185]
	v_rcp_f32_e32 v186, v161
	v_max_f32_e32 v161, v187, v187
	v_exp_f32_e32 v187, v163
	v_pk_mul_f32 v[26:27], v[26:27], v[184:185]
	v_pk_add_f32 v[184:185], v[188:189], 1.0 op_sel_hi:[1,0]
	v_cvt_pk_f32_fp8_sdwa v[188:189], v182 src0_sel:WORD_1
	v_med3_f32 v161, v161, s35, v177
	v_mul_f32_e32 v161, 0xbfb8aa3b, v161
	v_med3_f32 v178, v178, s35, v177
	v_exp_f32_e32 v163, v161
	v_add_f32_e32 v161, 1.0, v187
	v_mul_f32_e32 v178, 0xbfb8aa3b, v178
	v_pk_mul_f32 v[184:185], v[194:195], v[184:185]
	v_rcp_f32_e32 v187, v161
	v_max_f32_e32 v161, v188, v188
	v_exp_f32_e32 v188, v178
	v_pk_mul_f32 v[30:31], v[30:31], v[184:185]
	v_cvt_pk_f32_fp8_e32 v[184:185], v181
	v_med3_f32 v161, v161, s35, v177
	v_med3_f32 v179, v179, s35, v177
	v_mul_f32_e32 v161, 0xbfb8aa3b, v161
	v_mul_f32_e32 v179, 0xbfb8aa3b, v179
	v_pk_add_f32 v[162:163], v[162:163], 1.0 op_sel_hi:[1,0]
	v_exp_f32_e32 v178, v161
	v_add_f32_e32 v161, 1.0, v188
	v_max_f32_e32 v188, v189, v189
	v_exp_f32_e32 v189, v179
	v_pk_mul_f32 v[162:163], v[186:187], v[162:163]
	v_cvt_pk_f32_fp8_e32 v[190:191], v183
	v_pk_mul_f32 v[38:39], v[38:39], v[162:163]
	v_med3_f32 v162, v184, s35, v177
	v_med3_f32 v188, v188, s35, v177
	v_mul_f32_e32 v162, 0xbfb8aa3b, v162
	v_mul_f32_e32 v179, 0xbfb8aa3b, v188
	v_rcp_f32_e32 v188, v161
	v_add_f32_e32 v161, 1.0, v189
	v_exp_f32_e32 v163, v162
	v_exp_f32_e32 v179, v179
	v_rcp_f32_e32 v189, v161
	v_med3_f32 v161, v190, s35, v177
	v_mul_f32_e32 v161, 0xbfb8aa3b, v161
	v_exp_f32_e32 v162, v161
	v_add_f32_e32 v161, 1.0, v163
	v_cvt_pk_f32_fp8_sdwa v[180:181], v181 src0_sel:WORD_1
	v_pk_add_f32 v[178:179], v[178:179], 1.0 op_sel_hi:[1,0]
	v_med3_f32 v163, v185, s35, v177
	v_pk_mul_f32 v[178:179], v[188:189], v[178:179]
	v_mul_f32_e32 v163, 0xbfb8aa3b, v163
	v_pk_mul_f32 v[40:41], v[40:41], v[178:179]
	v_exp_f32_e32 v179, v163
	v_cvt_pk_f32_fp8_sdwa v[182:183], v183 src0_sel:WORD_1
	v_rcp_f32_e32 v178, v161
	v_med3_f32 v161, v191, s35, v177
	v_mul_f32_e32 v161, 0xbfb8aa3b, v161
	v_med3_f32 v180, v180, s35, v177
	v_exp_f32_e32 v163, v161
	v_add_f32_e32 v161, 1.0, v179
	v_mul_f32_e32 v180, 0xbfb8aa3b, v180
	v_rcp_f32_e32 v179, v161
	v_max_f32_e32 v161, v182, v182
	v_exp_f32_e32 v182, v180
	v_med3_f32 v161, v161, s35, v177
	v_med3_f32 v181, v181, s35, v177
	v_mul_f32_e32 v161, 0xbfb8aa3b, v161
	v_mul_f32_e32 v181, 0xbfb8aa3b, v181
	v_exp_f32_e32 v180, v161
	v_add_f32_e32 v161, 1.0, v182
	v_max_f32_e32 v182, v183, v183
	v_exp_f32_e32 v183, v181
	v_med3_f32 v182, v182, s35, v177
	v_mul_f32_e32 v181, 0xbfb8aa3b, v182
	v_exp_f32_e32 v181, v181
	v_rcp_f32_e32 v182, v161
	v_add_f32_e32 v161, 1.0, v183
	v_pk_add_f32 v[162:163], v[162:163], 1.0 op_sel_hi:[1,0]
	v_rcp_f32_e32 v183, v161
	v_pk_mul_f32 v[162:163], v[178:179], v[162:163]
	v_pk_add_f32 v[180:181], v[180:181], 1.0 op_sel_hi:[1,0]
	v_pk_mul_f32 v[42:43], v[42:43], v[162:163]
	s_waitcnt vmcnt(27)
	v_cvt_pk_f32_fp8_e32 v[162:163], v158
	v_pk_mul_f32 v[178:179], v[182:183], v[180:181]
	s_waitcnt vmcnt(26)
	v_cvt_pk_f32_fp8_e32 v[182:183], v156
	v_pk_mul_f32 v[44:45], v[44:45], v[178:179]
	v_med3_f32 v162, v162, s35, v177
	v_mul_f32_e32 v162, 0xbfb8aa3b, v162
	v_max_f32_e32 v161, v182, v182
	v_exp_f32_e32 v182, v162
	v_med3_f32 v161, v161, s35, v177
	v_cvt_pk_f32_fp8_sdwa v[178:179], v158 src0_sel:WORD_1
	v_mul_f32_e32 v161, 0xbfb8aa3b, v161
	v_med3_f32 v163, v163, s35, v177
	v_exp_f32_e32 v162, v161
	v_add_f32_e32 v161, 1.0, v182
	v_mul_f32_e32 v163, 0xbfb8aa3b, v163
	v_rcp_f32_e32 v182, v161
	v_max_f32_e32 v161, v183, v183
	v_exp_f32_e32 v183, v163
	v_cvt_pk_f32_fp8_sdwa v[184:185], v156 src0_sel:WORD_1
	v_med3_f32 v161, v161, s35, v177
	v_mul_f32_e32 v161, 0xbfb8aa3b, v161
	v_med3_f32 v178, v178, s35, v177
	v_exp_f32_e32 v163, v161
	v_add_f32_e32 v161, 1.0, v183
	v_mul_f32_e32 v178, 0xbfb8aa3b, v178
	v_rcp_f32_e32 v183, v161
	v_max_f32_e32 v161, v184, v184
	v_exp_f32_e32 v184, v178
	v_cvt_pk_f32_fp8_e32 v[180:181], v159
	v_med3_f32 v161, v161, s35, v177
	v_med3_f32 v179, v179, s35, v177
	v_mul_f32_e32 v161, 0xbfb8aa3b, v161
	v_mul_f32_e32 v179, 0xbfb8aa3b, v179
	v_pk_add_f32 v[162:163], v[162:163], 1.0 op_sel_hi:[1,0]
	v_cvt_pk_f32_fp8_sdwa v[158:159], v159 src0_sel:WORD_1
	v_exp_f32_e32 v178, v161
	v_add_f32_e32 v161, 1.0, v184
	v_max_f32_e32 v184, v185, v185
	v_exp_f32_e32 v185, v179
	v_pk_mul_f32 v[162:163], v[182:183], v[162:163]
	v_cvt_pk_f32_fp8_e32 v[186:187], v157
	v_pk_mul_f32 v[50:51], v[50:51], v[162:163]
	v_med3_f32 v162, v180, s35, v177
	v_med3_f32 v184, v184, s35, v177
	v_mul_f32_e32 v162, 0xbfb8aa3b, v162
	v_cvt_pk_f32_fp8_sdwa v[156:157], v157 src0_sel:WORD_1
	v_mul_f32_e32 v179, 0xbfb8aa3b, v184
	v_rcp_f32_e32 v184, v161
	v_add_f32_e32 v161, 1.0, v185
	v_exp_f32_e32 v163, v162
	v_exp_f32_e32 v179, v179
	v_rcp_f32_e32 v185, v161
	v_med3_f32 v158, v158, s35, v177
	v_med3_f32 v159, v159, s35, v177
	v_med3_f32 v161, v186, s35, v177
	v_mul_f32_e32 v158, 0xbfb8aa3b, v158
	v_mul_f32_e32 v159, 0xbfb8aa3b, v159
	v_mul_f32_e32 v161, 0xbfb8aa3b, v161
	v_exp_f32_e32 v158, v158
	v_exp_f32_e32 v159, v159
	v_exp_f32_e32 v162, v161
	v_add_f32_e32 v161, 1.0, v163
	v_pk_add_f32 v[178:179], v[178:179], 1.0 op_sel_hi:[1,0]
	v_med3_f32 v163, v181, s35, v177
	v_med3_f32 v156, v156, s35, v177
	v_med3_f32 v157, v157, s35, v177
	v_pk_mul_f32 v[178:179], v[184:185], v[178:179]
	v_mul_f32_e32 v163, 0xbfb8aa3b, v163
	v_mul_f32_e32 v156, 0xbfb8aa3b, v156
	v_mul_f32_e32 v157, 0xbfb8aa3b, v157
	v_pk_mul_f32 v[52:53], v[52:53], v[178:179]
	v_exp_f32_e32 v179, v163
	v_exp_f32_e32 v156, v156
	v_add_f32_e32 v158, 1.0, v158
	v_exp_f32_e32 v157, v157
	v_add_f32_e32 v159, 1.0, v159
	v_rcp_f32_e32 v178, v161
	v_rcp_f32_e32 v158, v158
	v_rcp_f32_e32 v159, v159
	v_med3_f32 v161, v187, s35, v177
	v_mul_f32_e32 v161, 0xbfb8aa3b, v161
	v_exp_f32_e32 v163, v161
	v_add_f32_e32 v161, 1.0, v179
	v_pk_add_f32 v[156:157], v[156:157], 1.0 op_sel_hi:[1,0]
	v_rcp_f32_e32 v179, v161
	v_pk_mul_f32 v[156:157], v[158:159], v[156:157]
	v_pk_add_f32 v[162:163], v[162:163], 1.0 op_sel_hi:[1,0]
	v_pk_mul_f32 v[56:57], v[56:57], v[156:157]
	s_waitcnt vmcnt(25)
	v_cvt_pk_f32_fp8_e32 v[156:157], v154
	v_pk_mul_f32 v[162:163], v[178:179], v[162:163]
	s_waitcnt vmcnt(24)
	v_cvt_pk_f32_fp8_e32 v[178:179], v152
	v_cvt_pk_f32_fp8_sdwa v[158:159], v154 src0_sel:WORD_1
	v_med3_f32 v156, v156, s35, v177
	v_mul_f32_e32 v156, 0xbfb8aa3b, v156
	v_max_f32_e32 v161, v178, v178
	v_exp_f32_e32 v178, v156
	v_med3_f32 v157, v157, s35, v177
	v_med3_f32 v156, v161, s35, v177
	v_add_f32_e32 v161, 1.0, v178
	v_mul_f32_e32 v157, 0xbfb8aa3b, v157
	v_rcp_f32_e32 v178, v161
	v_max_f32_e32 v161, v179, v179
	v_exp_f32_e32 v179, v157
	v_cvt_pk_f32_fp8_sdwa v[180:181], v152 src0_sel:WORD_1
	v_med3_f32 v158, v158, s35, v177
	v_med3_f32 v157, v161, s35, v177
	v_add_f32_e32 v161, 1.0, v179
	v_mul_f32_e32 v158, 0xbfb8aa3b, v158
	v_rcp_f32_e32 v179, v161
	v_max_f32_e32 v161, v180, v180
	v_exp_f32_e32 v180, v158
	v_med3_f32 v159, v159, s35, v177
	v_pk_mul_f32 v[54:55], v[54:55], v[162:163]
	v_cvt_pk_f32_fp8_e32 v[162:163], v155
	v_cvt_pk_f32_fp8_sdwa v[154:155], v155 src0_sel:WORD_1
	v_mul_f32_e32 v156, 0xbfb8aa3b, v156
	v_mul_f32_e32 v157, 0xbfb8aa3b, v157
	v_mul_f32_e32 v159, 0xbfb8aa3b, v159
	v_exp_f32_e32 v156, v156
	v_exp_f32_e32 v157, v157
	v_med3_f32 v158, v161, s35, v177
	v_add_f32_e32 v161, 1.0, v180
	v_max_f32_e32 v180, v181, v181
	v_exp_f32_e32 v181, v159
	v_med3_f32 v180, v180, s35, v177
	v_cvt_pk_f32_fp8_e32 v[182:183], v153
	v_cvt_pk_f32_fp8_sdwa v[152:153], v153 src0_sel:WORD_1
	v_mul_f32_e32 v158, 0xbfb8aa3b, v158
	v_mul_f32_e32 v159, 0xbfb8aa3b, v180
	v_exp_f32_e32 v158, v158
	v_exp_f32_e32 v159, v159
	v_rcp_f32_e32 v180, v161
	v_add_f32_e32 v161, 1.0, v181
	v_pk_add_f32 v[156:157], v[156:157], 1.0 op_sel_hi:[1,0]
	v_med3_f32 v154, v154, s35, v177
	v_med3_f32 v155, v155, s35, v177
	v_rcp_f32_e32 v181, v161
	v_pk_mul_f32 v[156:157], v[178:179], v[156:157]
	v_mul_f32_e32 v154, 0xbfb8aa3b, v154
	v_mul_f32_e32 v155, 0xbfb8aa3b, v155
	v_pk_mul_f32 v[62:63], v[62:63], v[156:157]
	v_exp_f32_e32 v154, v154
	v_exp_f32_e32 v155, v155
	v_med3_f32 v157, v162, s35, v177
	v_pk_add_f32 v[158:159], v[158:159], 1.0 op_sel_hi:[1,0]
	v_mul_f32_e32 v157, 0xbfb8aa3b, v157
	v_med3_f32 v152, v152, s35, v177
	v_med3_f32 v153, v153, s35, v177
	v_pk_mul_f32 v[158:159], v[180:181], v[158:159]
	v_exp_f32_e32 v157, v157
	v_mul_f32_e32 v152, 0xbfb8aa3b, v152
	v_mul_f32_e32 v153, 0xbfb8aa3b, v153
	v_pk_mul_f32 v[64:65], v[64:65], v[158:159]
	v_exp_f32_e32 v152, v152
	v_add_f32_e32 v154, 1.0, v154
	v_exp_f32_e32 v153, v153
	v_add_f32_e32 v155, 1.0, v155
	v_med3_f32 v159, v163, s35, v177
	v_rcp_f32_e32 v154, v154
	v_rcp_f32_e32 v155, v155
	v_mul_f32_e32 v159, 0xbfb8aa3b, v159
	v_add_f32_e32 v157, 1.0, v157
	v_exp_f32_e32 v159, v159
	v_rcp_f32_e32 v158, v157
	v_pk_add_f32 v[152:153], v[152:153], 1.0 op_sel_hi:[1,0]
	v_med3_f32 v156, v182, s35, v177
	v_med3_f32 v157, v183, s35, v177
	v_pk_mul_f32 v[152:153], v[154:155], v[152:153]
	v_mul_f32_e32 v156, 0xbfb8aa3b, v156
	v_mul_f32_e32 v157, 0xbfb8aa3b, v157
	v_pk_mul_f32 v[68:69], v[68:69], v[152:153]
	s_waitcnt vmcnt(23)
	v_cvt_pk_f32_fp8_e32 v[152:153], v150
	v_exp_f32_e32 v156, v156
	v_exp_f32_e32 v157, v157
	v_add_f32_e32 v159, 1.0, v159
	v_rcp_f32_e32 v159, v159
	v_pk_add_f32 v[156:157], v[156:157], 1.0 op_sel_hi:[1,0]
	v_med3_f32 v152, v152, s35, v177
	v_pk_mul_f32 v[156:157], v[158:159], v[156:157]
	s_waitcnt vmcnt(22)
	v_cvt_pk_f32_fp8_e32 v[158:159], v148
	v_mul_f32_e32 v152, 0xbfb8aa3b, v152
	v_exp_f32_e32 v161, v152
	v_cvt_pk_f32_fp8_sdwa v[154:155], v150 src0_sel:WORD_1
	v_med3_f32 v153, v153, s35, v177
	v_mul_f32_e32 v153, 0xbfb8aa3b, v153
	v_cvt_pk_f32_fp8_sdwa v[162:163], v148 src0_sel:WORD_1
	v_med3_f32 v152, v158, s35, v177
	v_add_f32_e32 v158, 1.0, v161
	v_exp_f32_e32 v161, v153
	v_med3_f32 v154, v154, s35, v177
	v_mul_f32_e32 v154, 0xbfb8aa3b, v154
	v_med3_f32 v153, v159, s35, v177
	v_add_f32_e32 v159, 1.0, v161
	v_max_f32_e32 v161, v162, v162
	v_exp_f32_e32 v162, v154
	v_med3_f32 v155, v155, s35, v177
	v_pk_mul_f32 v[66:67], v[66:67], v[156:157]
	v_cvt_pk_f32_fp8_e32 v[156:157], v151
	v_cvt_pk_f32_fp8_sdwa v[150:151], v151 src0_sel:WORD_1
	v_mul_f32_e32 v152, 0xbfb8aa3b, v152
	v_mul_f32_e32 v153, 0xbfb8aa3b, v153
	v_mul_f32_e32 v155, 0xbfb8aa3b, v155
	v_exp_f32_e32 v152, v152
	v_exp_f32_e32 v153, v153
	v_med3_f32 v154, v161, s35, v177
	v_add_f32_e32 v161, 1.0, v162
	v_max_f32_e32 v162, v163, v163
	v_exp_f32_e32 v163, v155
	v_rcp_f32_e32 v158, v158
	v_rcp_f32_e32 v159, v159
	v_med3_f32 v162, v162, s35, v177
	v_cvt_pk_f32_fp8_e32 v[178:179], v149
	v_cvt_pk_f32_fp8_sdwa v[148:149], v149 src0_sel:WORD_1
	v_mul_f32_e32 v154, 0xbfb8aa3b, v154
	v_mul_f32_e32 v155, 0xbfb8aa3b, v162
	v_exp_f32_e32 v154, v154
	v_exp_f32_e32 v155, v155
	v_rcp_f32_e32 v162, v161
	v_add_f32_e32 v161, 1.0, v163
	v_pk_add_f32 v[152:153], v[152:153], 1.0 op_sel_hi:[1,0]
	v_med3_f32 v150, v150, s35, v177
	v_med3_f32 v151, v151, s35, v177
	v_rcp_f32_e32 v163, v161
	v_pk_mul_f32 v[152:153], v[158:159], v[152:153]
	v_mul_f32_e32 v150, 0xbfb8aa3b, v150
	v_mul_f32_e32 v151, 0xbfb8aa3b, v151
	v_pk_mul_f32 v[74:75], v[74:75], v[152:153]
	v_exp_f32_e32 v150, v150
	v_exp_f32_e32 v151, v151
	v_med3_f32 v153, v156, s35, v177
	v_pk_add_f32 v[154:155], v[154:155], 1.0 op_sel_hi:[1,0]
	v_mul_f32_e32 v153, 0xbfb8aa3b, v153
	v_med3_f32 v148, v148, s35, v177
	v_med3_f32 v149, v149, s35, v177
	v_pk_mul_f32 v[154:155], v[162:163], v[154:155]
	v_exp_f32_e32 v153, v153
	v_mul_f32_e32 v148, 0xbfb8aa3b, v148
	v_mul_f32_e32 v149, 0xbfb8aa3b, v149
	v_pk_mul_f32 v[76:77], v[76:77], v[154:155]
	v_exp_f32_e32 v148, v148
	v_add_f32_e32 v150, 1.0, v150
	v_exp_f32_e32 v149, v149
	v_add_f32_e32 v151, 1.0, v151
	v_med3_f32 v155, v157, s35, v177
	v_rcp_f32_e32 v150, v150
	v_rcp_f32_e32 v151, v151
	v_mul_f32_e32 v155, 0xbfb8aa3b, v155
	v_add_f32_e32 v153, 1.0, v153
	v_exp_f32_e32 v155, v155
	v_rcp_f32_e32 v154, v153
	v_pk_add_f32 v[148:149], v[148:149], 1.0 op_sel_hi:[1,0]
	v_med3_f32 v152, v178, s35, v177
	v_med3_f32 v153, v179, s35, v177
	v_pk_mul_f32 v[148:149], v[150:151], v[148:149]
	v_mul_f32_e32 v152, 0xbfb8aa3b, v152
	v_mul_f32_e32 v153, 0xbfb8aa3b, v153
	v_pk_mul_f32 v[80:81], v[80:81], v[148:149]
	s_waitcnt vmcnt(21)
	v_cvt_pk_f32_fp8_e32 v[148:149], v146
	v_exp_f32_e32 v152, v152
	v_exp_f32_e32 v153, v153
	v_add_f32_e32 v155, 1.0, v155
	v_rcp_f32_e32 v155, v155
	v_pk_add_f32 v[152:153], v[152:153], 1.0 op_sel_hi:[1,0]
	v_med3_f32 v148, v148, s35, v177
	v_pk_mul_f32 v[152:153], v[154:155], v[152:153]
	s_waitcnt vmcnt(20)
	v_cvt_pk_f32_fp8_e32 v[154:155], v144
	v_mul_f32_e32 v148, 0xbfb8aa3b, v148
	v_exp_f32_e32 v161, v148
	v_cvt_pk_f32_fp8_sdwa v[150:151], v146 src0_sel:WORD_1
	v_med3_f32 v149, v149, s35, v177
	v_mul_f32_e32 v149, 0xbfb8aa3b, v149
	v_med3_f32 v148, v154, s35, v177
	v_add_f32_e32 v154, 1.0, v161
	v_exp_f32_e32 v161, v149
	v_med3_f32 v150, v150, s35, v177
	v_cvt_pk_f32_fp8_sdwa v[156:157], v144 src0_sel:WORD_1
	v_mul_f32_e32 v150, 0xbfb8aa3b, v150
	v_med3_f32 v149, v155, s35, v177
	v_add_f32_e32 v155, 1.0, v161
	v_exp_f32_e32 v161, v150
	v_med3_f32 v151, v151, s35, v177
	v_pk_mul_f32 v[78:79], v[78:79], v[152:153]
	v_cvt_pk_f32_fp8_e32 v[152:153], v147
	v_cvt_pk_f32_fp8_sdwa v[146:147], v147 src0_sel:WORD_1
	v_mul_f32_e32 v148, 0xbfb8aa3b, v148
	v_mul_f32_e32 v149, 0xbfb8aa3b, v149
	v_mul_f32_e32 v151, 0xbfb8aa3b, v151
	v_exp_f32_e32 v148, v148
	v_exp_f32_e32 v149, v149
	v_med3_f32 v150, v156, s35, v177
	v_add_f32_e32 v156, 1.0, v161
	v_exp_f32_e32 v161, v151
	v_rcp_f32_e32 v154, v154
	v_rcp_f32_e32 v155, v155
	v_med3_f32 v157, v157, s35, v177
	v_cvt_pk_f32_fp8_e32 v[158:159], v145
	v_cvt_pk_f32_fp8_sdwa v[144:145], v145 src0_sel:WORD_1
	v_mul_f32_e32 v150, 0xbfb8aa3b, v150
	v_mul_f32_e32 v151, 0xbfb8aa3b, v157
	v_exp_f32_e32 v150, v150
	v_exp_f32_e32 v151, v151
	v_add_f32_e32 v157, 1.0, v161
	v_pk_add_f32 v[148:149], v[148:149], 1.0 op_sel_hi:[1,0]
	v_med3_f32 v146, v146, s35, v177
	v_med3_f32 v147, v147, s35, v177
	v_rcp_f32_e32 v156, v156
	v_rcp_f32_e32 v157, v157
	v_pk_mul_f32 v[148:149], v[154:155], v[148:149]
	v_mul_f32_e32 v146, 0xbfb8aa3b, v146
	v_mul_f32_e32 v147, 0xbfb8aa3b, v147
	v_pk_mul_f32 v[82:83], v[82:83], v[148:149]
	v_exp_f32_e32 v146, v146
	v_exp_f32_e32 v147, v147
	v_med3_f32 v149, v152, s35, v177
	v_pk_add_f32 v[150:151], v[150:151], 1.0 op_sel_hi:[1,0]
	v_mul_f32_e32 v149, 0xbfb8aa3b, v149
	v_med3_f32 v144, v144, s35, v177
	v_med3_f32 v145, v145, s35, v177
	v_pk_mul_f32 v[150:151], v[156:157], v[150:151]
	v_exp_f32_e32 v149, v149
	v_mul_f32_e32 v144, 0xbfb8aa3b, v144
	v_mul_f32_e32 v145, 0xbfb8aa3b, v145
	v_pk_mul_f32 v[84:85], v[84:85], v[150:151]
	v_exp_f32_e32 v144, v144
	v_add_f32_e32 v146, 1.0, v146
	v_exp_f32_e32 v145, v145
	v_add_f32_e32 v147, 1.0, v147
	v_med3_f32 v151, v153, s35, v177
	v_rcp_f32_e32 v146, v146
	v_rcp_f32_e32 v147, v147
	v_mul_f32_e32 v151, 0xbfb8aa3b, v151
	v_add_f32_e32 v149, 1.0, v149
	v_exp_f32_e32 v151, v151
	v_rcp_f32_e32 v150, v149
	v_pk_add_f32 v[144:145], v[144:145], 1.0 op_sel_hi:[1,0]
	v_med3_f32 v148, v158, s35, v177
	v_med3_f32 v149, v159, s35, v177
	v_pk_mul_f32 v[144:145], v[146:147], v[144:145]
	v_mul_f32_e32 v148, 0xbfb8aa3b, v148
	v_mul_f32_e32 v149, 0xbfb8aa3b, v149
	v_pk_mul_f32 v[92:93], v[92:93], v[144:145]
	s_waitcnt vmcnt(19)
	v_cvt_pk_f32_fp8_e32 v[144:145], v142
	v_exp_f32_e32 v148, v148
	v_exp_f32_e32 v149, v149
	v_add_f32_e32 v151, 1.0, v151
	v_rcp_f32_e32 v151, v151
	v_pk_add_f32 v[148:149], v[148:149], 1.0 op_sel_hi:[1,0]
	v_med3_f32 v144, v144, s35, v177
	v_pk_mul_f32 v[148:149], v[150:151], v[148:149]
	s_waitcnt vmcnt(18)
	v_cvt_pk_f32_fp8_e32 v[150:151], v140
	v_mul_f32_e32 v144, 0xbfb8aa3b, v144
	v_exp_f32_e32 v156, v144
	v_cvt_pk_f32_fp8_sdwa v[146:147], v142 src0_sel:WORD_1
	v_med3_f32 v145, v145, s35, v177
	v_mul_f32_e32 v145, 0xbfb8aa3b, v145
	v_med3_f32 v144, v150, s35, v177
	v_add_f32_e32 v150, 1.0, v156
	v_exp_f32_e32 v156, v145
	v_med3_f32 v146, v146, s35, v177
	v_cvt_pk_f32_fp8_sdwa v[152:153], v140 src0_sel:WORD_1
	v_mul_f32_e32 v146, 0xbfb8aa3b, v146
	v_med3_f32 v145, v151, s35, v177
	v_add_f32_e32 v151, 1.0, v156
	v_exp_f32_e32 v156, v146
	v_med3_f32 v147, v147, s35, v177
	v_pk_mul_f32 v[90:91], v[90:91], v[148:149]
	v_cvt_pk_f32_fp8_e32 v[148:149], v143
	v_cvt_pk_f32_fp8_sdwa v[142:143], v143 src0_sel:WORD_1
	v_mul_f32_e32 v144, 0xbfb8aa3b, v144
	v_mul_f32_e32 v145, 0xbfb8aa3b, v145
	v_mul_f32_e32 v147, 0xbfb8aa3b, v147
	v_exp_f32_e32 v144, v144
	v_exp_f32_e32 v145, v145
	v_med3_f32 v146, v152, s35, v177
	v_add_f32_e32 v152, 1.0, v156
	v_exp_f32_e32 v156, v147
	v_rcp_f32_e32 v150, v150
	v_rcp_f32_e32 v151, v151
	v_med3_f32 v153, v153, s35, v177
	v_cvt_pk_f32_fp8_e32 v[154:155], v141
	v_cvt_pk_f32_fp8_sdwa v[140:141], v141 src0_sel:WORD_1
	v_mul_f32_e32 v146, 0xbfb8aa3b, v146
	v_mul_f32_e32 v147, 0xbfb8aa3b, v153
	v_exp_f32_e32 v146, v146
	v_exp_f32_e32 v147, v147
	v_add_f32_e32 v153, 1.0, v156
	v_pk_add_f32 v[144:145], v[144:145], 1.0 op_sel_hi:[1,0]
	v_med3_f32 v142, v142, s35, v177
	v_med3_f32 v143, v143, s35, v177
	v_rcp_f32_e32 v152, v152
	v_rcp_f32_e32 v153, v153
	v_pk_mul_f32 v[144:145], v[150:151], v[144:145]
	v_mul_f32_e32 v142, 0xbfb8aa3b, v142
	v_mul_f32_e32 v143, 0xbfb8aa3b, v143
	v_pk_mul_f32 v[94:95], v[94:95], v[144:145]
	v_exp_f32_e32 v142, v142
	v_exp_f32_e32 v143, v143
	v_med3_f32 v145, v148, s35, v177
	v_pk_add_f32 v[146:147], v[146:147], 1.0 op_sel_hi:[1,0]
	v_mul_f32_e32 v145, 0xbfb8aa3b, v145
	v_med3_f32 v140, v140, s35, v177
	v_med3_f32 v141, v141, s35, v177
	v_pk_mul_f32 v[146:147], v[152:153], v[146:147]
	v_exp_f32_e32 v145, v145
	v_mul_f32_e32 v140, 0xbfb8aa3b, v140
	v_mul_f32_e32 v141, 0xbfb8aa3b, v141
	v_pk_mul_f32 v[96:97], v[96:97], v[146:147]
	v_exp_f32_e32 v140, v140
	v_add_f32_e32 v142, 1.0, v142
	v_exp_f32_e32 v141, v141
	v_add_f32_e32 v143, 1.0, v143
	v_med3_f32 v147, v149, s35, v177
	v_rcp_f32_e32 v142, v142
	v_rcp_f32_e32 v143, v143
	v_mul_f32_e32 v147, 0xbfb8aa3b, v147
	v_add_f32_e32 v145, 1.0, v145
	v_exp_f32_e32 v147, v147
	v_rcp_f32_e32 v146, v145
	v_pk_add_f32 v[140:141], v[140:141], 1.0 op_sel_hi:[1,0]
	v_med3_f32 v144, v154, s35, v177
	v_med3_f32 v145, v155, s35, v177
	v_pk_mul_f32 v[140:141], v[142:143], v[140:141]
	v_mul_f32_e32 v144, 0xbfb8aa3b, v144
	v_mul_f32_e32 v145, 0xbfb8aa3b, v145
	v_pk_mul_f32 v[104:105], v[104:105], v[140:141]
	s_waitcnt vmcnt(17)
	v_cvt_pk_f32_fp8_e32 v[140:141], v138
	v_exp_f32_e32 v144, v144
	v_exp_f32_e32 v145, v145
	v_add_f32_e32 v147, 1.0, v147
	v_rcp_f32_e32 v147, v147
	v_pk_add_f32 v[144:145], v[144:145], 1.0 op_sel_hi:[1,0]
	v_med3_f32 v140, v140, s35, v177
	v_pk_mul_f32 v[144:145], v[146:147], v[144:145]
	s_waitcnt vmcnt(16)
	v_cvt_pk_f32_fp8_e32 v[146:147], v136
	v_mul_f32_e32 v140, 0xbfb8aa3b, v140
	v_exp_f32_e32 v152, v140
	v_cvt_pk_f32_fp8_sdwa v[142:143], v138 src0_sel:WORD_1
	v_med3_f32 v141, v141, s35, v177
	v_mul_f32_e32 v141, 0xbfb8aa3b, v141
	v_med3_f32 v140, v146, s35, v177
	v_add_f32_e32 v146, 1.0, v152
	v_exp_f32_e32 v152, v141
	v_med3_f32 v142, v142, s35, v177
	v_cvt_pk_f32_fp8_sdwa v[148:149], v136 src0_sel:WORD_1
	v_mul_f32_e32 v142, 0xbfb8aa3b, v142
	v_med3_f32 v141, v147, s35, v177
	v_add_f32_e32 v147, 1.0, v152
	v_exp_f32_e32 v152, v142
	v_med3_f32 v143, v143, s35, v177
	v_mul_f32_e32 v140, 0xbfb8aa3b, v140
	v_mul_f32_e32 v141, 0xbfb8aa3b, v141
	v_mul_f32_e32 v143, 0xbfb8aa3b, v143
	v_exp_f32_e32 v140, v140
	v_exp_f32_e32 v141, v141
	v_med3_f32 v142, v148, s35, v177
	v_add_f32_e32 v148, 1.0, v152
	v_exp_f32_e32 v152, v143
	v_rcp_f32_e32 v146, v146
	v_rcp_f32_e32 v147, v147
	v_pk_mul_f32 v[102:103], v[102:103], v[144:145]
	v_cvt_pk_f32_fp8_e32 v[144:145], v139
	v_med3_f32 v149, v149, s35, v177
	v_mul_f32_e32 v142, 0xbfb8aa3b, v142
	v_mul_f32_e32 v143, 0xbfb8aa3b, v149
	v_exp_f32_e32 v142, v142
	v_exp_f32_e32 v143, v143
	v_add_f32_e32 v149, 1.0, v152
	v_pk_add_f32 v[140:141], v[140:141], 1.0 op_sel_hi:[1,0]
	v_rcp_f32_e32 v148, v148
	v_rcp_f32_e32 v149, v149
	v_pk_mul_f32 v[140:141], v[146:147], v[140:141]
	v_cvt_pk_f32_fp8_sdwa v[138:139], v139 src0_sel:WORD_1
	v_pk_mul_f32 v[106:107], v[106:107], v[140:141]
	v_med3_f32 v141, v144, s35, v177
	v_pk_add_f32 v[142:143], v[142:143], 1.0 op_sel_hi:[1,0]
	v_mul_f32_e32 v141, 0xbfb8aa3b, v141
	v_pk_mul_f32 v[142:143], v[148:149], v[142:143]
	v_exp_f32_e32 v141, v141
	v_cvt_pk_f32_fp8_e32 v[150:151], v137
	v_cvt_pk_f32_fp8_sdwa v[136:137], v137 src0_sel:WORD_1
	v_pk_mul_f32 v[108:109], v[108:109], v[142:143]
	v_med3_f32 v143, v145, s35, v177
	v_med3_f32 v138, v138, s35, v177
	v_med3_f32 v139, v139, s35, v177
	v_mul_f32_e32 v143, 0xbfb8aa3b, v143
	v_mul_f32_e32 v138, 0xbfb8aa3b, v138
	v_mul_f32_e32 v139, 0xbfb8aa3b, v139
	v_add_f32_e32 v141, 1.0, v141
	v_exp_f32_e32 v143, v143
	v_exp_f32_e32 v138, v138
	v_exp_f32_e32 v139, v139
	v_rcp_f32_e32 v142, v141
	v_med3_f32 v140, v150, s35, v177
	v_med3_f32 v141, v151, s35, v177
	v_med3_f32 v136, v136, s35, v177
	v_med3_f32 v137, v137, s35, v177
	v_mul_f32_e32 v140, 0xbfb8aa3b, v140
	v_mul_f32_e32 v141, 0xbfb8aa3b, v141
	v_mul_f32_e32 v136, 0xbfb8aa3b, v136
	v_mul_f32_e32 v137, 0xbfb8aa3b, v137
	v_exp_f32_e32 v140, v140
	v_exp_f32_e32 v141, v141
	v_add_f32_e32 v143, 1.0, v143
	v_exp_f32_e32 v136, v136
	v_add_f32_e32 v138, 1.0, v138
	v_exp_f32_e32 v137, v137
	v_add_f32_e32 v139, 1.0, v139
	v_rcp_f32_e32 v143, v143
	v_rcp_f32_e32 v138, v138
	v_rcp_f32_e32 v139, v139
	v_pk_add_f32 v[136:137], v[136:137], 1.0 op_sel_hi:[1,0]
	v_pk_add_f32 v[140:141], v[140:141], 1.0 op_sel_hi:[1,0]
	v_pk_mul_f32 v[136:137], v[138:139], v[136:137]
	v_pk_mul_f32 v[140:141], v[142:143], v[140:141]
	v_pk_mul_f32 v[116:117], v[116:117], v[136:137]
	v_pk_mul_f32 v[114:115], v[114:115], v[140:141]
	s_nop 0
	s_waitcnt vmcnt(0)
	v_mov_b64_e32 v[162:163], v[220:221]
	v_mov_b64_e32 v[160:161], v[222:223]
	v_mov_b64_e32 v[178:179], v[224:225]
	v_mov_b64_e32 v[180:181], v[226:227]
	v_mov_b64_e32 v[158:159], v[228:229]
	v_mov_b64_e32 v[156:157], v[230:231]
	v_mov_b64_e32 v[154:155], v[232:233]
	v_mov_b64_e32 v[152:153], v[234:235]
	v_mov_b64_e32 v[150:151], v[236:237]
	v_mov_b64_e32 v[148:149], v[238:239]
	v_mov_b64_e32 v[146:147], v[240:241]
	v_mov_b64_e32 v[144:145], v[242:243]
	v_mov_b64_e32 v[142:143], v[244:245]
	v_mov_b64_e32 v[140:141], v[246:247]
	v_mov_b64_e32 v[138:139], v[248:249]
	v_mov_b64_e32 v[136:137], v[250:251]
	v_lshl_add_u32 v252, s23, 8, v214
	s_lshl_b32 s32, s60, 18
	v_add_u32_e32 v252, s32, v252
	global_load_dwordx2 v[220:221], v252, s[16:17]
	global_load_dwordx2 v[224:225], v252, s[16:17] offset:512
	global_load_dwordx2 v[228:229], v252, s[16:17] offset:1024
	global_load_dwordx2 v[232:233], v252, s[16:17] offset:1536
	global_load_dwordx2 v[236:237], v252, s[16:17] offset:2048
	global_load_dwordx2 v[240:241], v252, s[16:17] offset:2560
	global_load_dwordx2 v[244:245], v252, s[16:17] offset:3072
	global_load_dwordx2 v[248:249], v252, s[16:17] offset:3584
	v_cvt_pk_f32_fp8_e32 v[182:183], v162
	v_cvt_pk_f32_fp8_e32 v[188:189], v160
	v_cvt_pk_f32_fp8_sdwa v[184:185], v162 src0_sel:WORD_1
	v_cvt_pk_f32_fp8_sdwa v[190:191], v160 src0_sel:WORD_1
	v_med3_f32 v182, v182, s35, v177
	v_mul_f32_e32 v182, 0xbfb8aa3b, v182
	v_max_f32_e32 v134, v188, v188
	v_exp_f32_e32 v188, v182
	v_med3_f32 v134, v134, s35, v177
	v_mul_f32_e32 v134, 0xbfb8aa3b, v134
	v_med3_f32 v183, v183, s35, v177
	v_exp_f32_e32 v182, v134
	v_add_f32_e32 v134, 1.0, v188
	v_mul_f32_e32 v183, 0xbfb8aa3b, v183
	v_rcp_f32_e32 v188, v134
	v_max_f32_e32 v134, v189, v189
	v_exp_f32_e32 v189, v183
	v_med3_f32 v134, v134, s35, v177
	v_mul_f32_e32 v134, 0xbfb8aa3b, v134
	v_med3_f32 v184, v184, s35, v177
	v_exp_f32_e32 v183, v134
	v_add_f32_e32 v134, 1.0, v189
	v_mul_f32_e32 v184, 0xbfb8aa3b, v184
	v_rcp_f32_e32 v189, v134
	v_max_f32_e32 v134, v190, v190
	v_exp_f32_e32 v190, v184
	v_cvt_pk_f32_fp8_e32 v[186:187], v163
	v_med3_f32 v134, v134, s35, v177
	v_med3_f32 v185, v185, s35, v177
	v_mul_f32_e32 v134, 0xbfb8aa3b, v134
	v_mul_f32_e32 v185, 0xbfb8aa3b, v185
	v_pk_add_f32 v[182:183], v[182:183], 1.0 op_sel_hi:[1,0]
	v_exp_f32_e32 v184, v134
	v_add_f32_e32 v134, 1.0, v190
	v_max_f32_e32 v190, v191, v191
	v_exp_f32_e32 v191, v185
	v_pk_mul_f32 v[182:183], v[188:189], v[182:183]
	v_cvt_pk_f32_fp8_e32 v[192:193], v161
	v_pk_mul_f32 v[118:119], v[118:119], v[182:183]
	v_med3_f32 v182, v186, s35, v177
	v_med3_f32 v190, v190, s35, v177
	v_mul_f32_e32 v182, 0xbfb8aa3b, v182
	v_mul_f32_e32 v185, 0xbfb8aa3b, v190
	v_rcp_f32_e32 v190, v134
	v_add_f32_e32 v134, 1.0, v191
	v_exp_f32_e32 v183, v182
	v_exp_f32_e32 v185, v185
	v_rcp_f32_e32 v191, v134
	v_med3_f32 v134, v192, s35, v177
	v_mul_f32_e32 v134, 0xbfb8aa3b, v134
	v_exp_f32_e32 v182, v134
	v_add_f32_e32 v134, 1.0, v183
	v_pk_add_f32 v[184:185], v[184:185], 1.0 op_sel_hi:[1,0]
	v_med3_f32 v183, v187, s35, v177
	v_pk_mul_f32 v[184:185], v[190:191], v[184:185]
	v_mul_f32_e32 v183, 0xbfb8aa3b, v183
	v_pk_mul_f32 v[120:121], v[120:121], v[184:185]
	v_exp_f32_e32 v185, v183
	v_cvt_pk_f32_fp8_sdwa v[162:163], v163 src0_sel:WORD_1
	v_cvt_pk_f32_fp8_sdwa v[160:161], v161 src0_sel:WORD_1
	v_rcp_f32_e32 v184, v134
	v_med3_f32 v134, v193, s35, v177
	v_mul_f32_e32 v134, 0xbfb8aa3b, v134
	v_exp_f32_e32 v183, v134
	v_add_f32_e32 v134, 1.0, v185
	v_rcp_f32_e32 v185, v134
	v_max_f32_e32 v134, v160, v160
	v_med3_f32 v160, v162, s35, v177
	v_mul_f32_e32 v160, 0xbfb8aa3b, v160
	v_exp_f32_e32 v162, v160
	v_med3_f32 v134, v134, s35, v177
	v_mul_f32_e32 v134, 0xbfb8aa3b, v134
	v_exp_f32_e32 v160, v134
	v_add_f32_e32 v134, 1.0, v162
	v_med3_f32 v162, v163, s35, v177
	v_mul_f32_e32 v162, 0xbfb8aa3b, v162
	v_exp_f32_e32 v163, v162
	v_med3_f32 v161, v161, s35, v177
	v_mul_f32_e32 v161, 0xbfb8aa3b, v161
	v_exp_f32_e32 v161, v161
	v_rcp_f32_e32 v162, v134
	v_add_f32_e32 v134, 1.0, v163
	v_rcp_f32_e32 v163, v134
	v_pk_add_f32 v[160:161], v[160:161], 1.0 op_sel_hi:[1,0]
	v_pk_add_f32 v[182:183], v[182:183], 1.0 op_sel_hi:[1,0]
	v_cvt_pk_f32_fp8_sdwa v[186:187], v180 src0_sel:WORD_1
	v_pk_mul_f32 v[160:161], v[162:163], v[160:161]
	v_pk_mul_f32 v[182:183], v[184:185], v[182:183]
	v_pk_mul_f32 v[128:129], v[128:129], v[160:161]
	v_cvt_pk_f32_fp8_e32 v[160:161], v178
	v_cvt_pk_f32_fp8_e32 v[184:185], v180
	v_cvt_pk_f32_fp8_sdwa v[162:163], v178 src0_sel:WORD_1
	v_pk_mul_f32 v[126:127], v[126:127], v[182:183]
	v_med3_f32 v160, v160, s35, v177
	v_mul_f32_e32 v160, 0xbfb8aa3b, v160
	v_max_f32_e32 v134, v184, v184
	v_exp_f32_e32 v184, v160
	v_med3_f32 v134, v134, s35, v177
	v_mul_f32_e32 v134, 0xbfb8aa3b, v134
	v_med3_f32 v161, v161, s35, v177
	v_exp_f32_e32 v160, v134
	v_add_f32_e32 v134, 1.0, v184
	v_mul_f32_e32 v161, 0xbfb8aa3b, v161
	v_rcp_f32_e32 v184, v134
	v_max_f32_e32 v134, v185, v185
	v_exp_f32_e32 v185, v161
	v_med3_f32 v134, v134, s35, v177
	v_mul_f32_e32 v134, 0xbfb8aa3b, v134
	v_med3_f32 v162, v162, s35, v177
	v_exp_f32_e32 v161, v134
	v_add_f32_e32 v134, 1.0, v185
	v_mul_f32_e32 v162, 0xbfb8aa3b, v162
	v_rcp_f32_e32 v185, v134
	v_max_f32_e32 v134, v186, v186
	v_exp_f32_e32 v186, v162
	v_cvt_pk_f32_fp8_e32 v[182:183], v179
	v_med3_f32 v134, v134, s35, v177
	v_med3_f32 v163, v163, s35, v177
	v_mul_f32_e32 v134, 0xbfb8aa3b, v134
	v_mul_f32_e32 v163, 0xbfb8aa3b, v163
	v_pk_add_f32 v[160:161], v[160:161], 1.0 op_sel_hi:[1,0]
	v_exp_f32_e32 v162, v134
	v_add_f32_e32 v134, 1.0, v186
	v_max_f32_e32 v186, v187, v187
	v_exp_f32_e32 v187, v163
	v_pk_mul_f32 v[160:161], v[184:185], v[160:161]
	v_cvt_pk_f32_fp8_e32 v[188:189], v181
	v_pk_mul_f32 v[122:123], v[122:123], v[160:161]
	v_med3_f32 v160, v182, s35, v177
	v_med3_f32 v186, v186, s35, v177
	v_mul_f32_e32 v160, 0xbfb8aa3b, v160
	v_mul_f32_e32 v163, 0xbfb8aa3b, v186
	v_rcp_f32_e32 v186, v134
	v_add_f32_e32 v134, 1.0, v187
	v_exp_f32_e32 v161, v160
	v_exp_f32_e32 v163, v163
	v_rcp_f32_e32 v187, v134
	v_med3_f32 v134, v188, s35, v177
	v_mul_f32_e32 v134, 0xbfb8aa3b, v134
	v_exp_f32_e32 v160, v134
	v_add_f32_e32 v134, 1.0, v161
	v_cvt_pk_f32_fp8_sdwa v[178:179], v179 src0_sel:WORD_1
	v_pk_add_f32 v[162:163], v[162:163], 1.0 op_sel_hi:[1,0]
	v_med3_f32 v161, v183, s35, v177
	v_pk_mul_f32 v[162:163], v[186:187], v[162:163]
	v_mul_f32_e32 v161, 0xbfb8aa3b, v161
	v_pk_mul_f32 v[124:125], v[124:125], v[162:163]
	v_exp_f32_e32 v163, v161
	v_cvt_pk_f32_fp8_sdwa v[180:181], v181 src0_sel:WORD_1
	v_rcp_f32_e32 v162, v134
	v_med3_f32 v134, v189, s35, v177
	v_mul_f32_e32 v134, 0xbfb8aa3b, v134
	v_med3_f32 v178, v178, s35, v177
	v_exp_f32_e32 v161, v134
	v_add_f32_e32 v134, 1.0, v163
	v_mul_f32_e32 v178, 0xbfb8aa3b, v178
	v_rcp_f32_e32 v163, v134
	v_max_f32_e32 v134, v180, v180
	v_exp_f32_e32 v180, v178
	v_med3_f32 v134, v134, s35, v177
	v_med3_f32 v179, v179, s35, v177
	v_mul_f32_e32 v134, 0xbfb8aa3b, v134
	v_mul_f32_e32 v179, 0xbfb8aa3b, v179
	v_exp_f32_e32 v178, v134
	v_add_f32_e32 v134, 1.0, v180
	v_max_f32_e32 v180, v181, v181
	v_exp_f32_e32 v181, v179
	v_med3_f32 v180, v180, s35, v177
	v_mul_f32_e32 v179, 0xbfb8aa3b, v180
	v_exp_f32_e32 v179, v179
	v_rcp_f32_e32 v180, v134
	v_add_f32_e32 v134, 1.0, v181
	v_pk_add_f32 v[160:161], v[160:161], 1.0 op_sel_hi:[1,0]
	v_rcp_f32_e32 v181, v134
	v_pk_mul_f32 v[160:161], v[162:163], v[160:161]
	v_pk_add_f32 v[178:179], v[178:179], 1.0 op_sel_hi:[1,0]
	v_pk_mul_f32 v[110:111], v[110:111], v[160:161]
	v_cvt_pk_f32_fp8_e32 v[160:161], v158
	v_pk_mul_f32 v[162:163], v[180:181], v[178:179]
	v_cvt_pk_f32_fp8_e32 v[180:181], v156
	v_pk_mul_f32 v[112:113], v[112:113], v[162:163]
	v_med3_f32 v160, v160, s35, v177
	v_mul_f32_e32 v160, 0xbfb8aa3b, v160
	v_max_f32_e32 v134, v180, v180
	v_exp_f32_e32 v180, v160
	v_med3_f32 v134, v134, s35, v177
	v_cvt_pk_f32_fp8_sdwa v[162:163], v158 src0_sel:WORD_1
	v_mul_f32_e32 v134, 0xbfb8aa3b, v134
	v_med3_f32 v161, v161, s35, v177
	v_exp_f32_e32 v160, v134
	v_add_f32_e32 v134, 1.0, v180
	v_mul_f32_e32 v161, 0xbfb8aa3b, v161
	v_rcp_f32_e32 v180, v134
	v_max_f32_e32 v134, v181, v181
	v_exp_f32_e32 v181, v161
	v_cvt_pk_f32_fp8_sdwa v[182:183], v156 src0_sel:WORD_1
	v_med3_f32 v134, v134, s35, v177
	v_mul_f32_e32 v134, 0xbfb8aa3b, v134
	v_med3_f32 v162, v162, s35, v177
	v_exp_f32_e32 v161, v134
	v_add_f32_e32 v134, 1.0, v181
	v_mul_f32_e32 v162, 0xbfb8aa3b, v162
	v_rcp_f32_e32 v181, v134
	v_max_f32_e32 v134, v182, v182
	v_exp_f32_e32 v182, v162
	v_cvt_pk_f32_fp8_e32 v[178:179], v159
	v_med3_f32 v134, v134, s35, v177
	v_med3_f32 v163, v163, s35, v177
	v_mul_f32_e32 v134, 0xbfb8aa3b, v134
	v_mul_f32_e32 v163, 0xbfb8aa3b, v163
	v_pk_add_f32 v[160:161], v[160:161], 1.0 op_sel_hi:[1,0]
	v_exp_f32_e32 v162, v134
	v_add_f32_e32 v134, 1.0, v182
	v_max_f32_e32 v182, v183, v183
	v_exp_f32_e32 v183, v163
	v_pk_mul_f32 v[160:161], v[180:181], v[160:161]
	v_cvt_pk_f32_fp8_e32 v[184:185], v157
	v_pk_mul_f32 v[98:99], v[98:99], v[160:161]
	v_med3_f32 v160, v178, s35, v177
	v_med3_f32 v182, v182, s35, v177
	v_mul_f32_e32 v160, 0xbfb8aa3b, v160
	v_mul_f32_e32 v163, 0xbfb8aa3b, v182
	v_rcp_f32_e32 v182, v134
	v_add_f32_e32 v134, 1.0, v183
	v_exp_f32_e32 v161, v160
	v_exp_f32_e32 v163, v163
	v_rcp_f32_e32 v183, v134
	v_med3_f32 v134, v184, s35, v177
	v_mul_f32_e32 v134, 0xbfb8aa3b, v134
	v_exp_f32_e32 v160, v134
	v_add_f32_e32 v134, 1.0, v161
	v_pk_add_f32 v[162:163], v[162:163], 1.0 op_sel_hi:[1,0]
	v_med3_f32 v161, v179, s35, v177
	v_pk_mul_f32 v[162:163], v[182:183], v[162:163]
	v_mul_f32_e32 v161, 0xbfb8aa3b, v161
	v_pk_mul_f32 v[100:101], v[100:101], v[162:163]
	v_exp_f32_e32 v163, v161
	v_cvt_pk_f32_fp8_sdwa v[158:159], v159 src0_sel:WORD_1
	v_cvt_pk_f32_fp8_sdwa v[156:157], v157 src0_sel:WORD_1
	v_rcp_f32_e32 v162, v134
	v_med3_f32 v134, v185, s35, v177
	v_mul_f32_e32 v134, 0xbfb8aa3b, v134
	v_exp_f32_e32 v161, v134
	v_add_f32_e32 v134, 1.0, v163
	v_rcp_f32_e32 v163, v134
	v_max_f32_e32 v134, v156, v156
	v_med3_f32 v156, v158, s35, v177
	v_mul_f32_e32 v156, 0xbfb8aa3b, v156
	v_exp_f32_e32 v158, v156
	v_med3_f32 v134, v134, s35, v177
	v_mul_f32_e32 v134, 0xbfb8aa3b, v134
	v_exp_f32_e32 v156, v134
	v_add_f32_e32 v134, 1.0, v158
	v_med3_f32 v158, v159, s35, v177
	v_mul_f32_e32 v158, 0xbfb8aa3b, v158
	v_exp_f32_e32 v159, v158
	v_med3_f32 v157, v157, s35, v177
	v_mul_f32_e32 v157, 0xbfb8aa3b, v157
	v_exp_f32_e32 v157, v157
	v_rcp_f32_e32 v158, v134
	v_add_f32_e32 v134, 1.0, v159
	v_rcp_f32_e32 v159, v134
	v_pk_add_f32 v[156:157], v[156:157], 1.0 op_sel_hi:[1,0]
	v_pk_add_f32 v[160:161], v[160:161], 1.0 op_sel_hi:[1,0]
	v_cvt_pk_f32_fp8_sdwa v[178:179], v152 src0_sel:WORD_1
	v_pk_mul_f32 v[156:157], v[158:159], v[156:157]
	v_pk_mul_f32 v[160:161], v[162:163], v[160:161]
	v_pk_mul_f32 v[88:89], v[88:89], v[156:157]
	v_cvt_pk_f32_fp8_e32 v[156:157], v154
	v_cvt_pk_f32_fp8_e32 v[162:163], v152
	v_cvt_pk_f32_fp8_sdwa v[158:159], v154 src0_sel:WORD_1
	v_pk_mul_f32 v[86:87], v[86:87], v[160:161]
	v_med3_f32 v156, v156, s35, v177
	v_mul_f32_e32 v156, 0xbfb8aa3b, v156
	v_max_f32_e32 v134, v162, v162
	v_exp_f32_e32 v162, v156
	v_med3_f32 v134, v134, s35, v177
	v_mul_f32_e32 v134, 0xbfb8aa3b, v134
	v_med3_f32 v157, v157, s35, v177
	v_exp_f32_e32 v156, v134
	v_add_f32_e32 v134, 1.0, v162
	v_mul_f32_e32 v157, 0xbfb8aa3b, v157
	v_rcp_f32_e32 v162, v134
	v_max_f32_e32 v134, v163, v163
	v_exp_f32_e32 v163, v157
	v_med3_f32 v134, v134, s35, v177
	v_mul_f32_e32 v134, 0xbfb8aa3b, v134
	v_med3_f32 v158, v158, s35, v177
	v_exp_f32_e32 v157, v134
	v_add_f32_e32 v134, 1.0, v163
	v_mul_f32_e32 v158, 0xbfb8aa3b, v158
	v_rcp_f32_e32 v163, v134
	v_max_f32_e32 v134, v178, v178
	v_exp_f32_e32 v178, v158
	v_cvt_pk_f32_fp8_e32 v[160:161], v155
	v_med3_f32 v134, v134, s35, v177
	v_med3_f32 v159, v159, s35, v177
	v_mul_f32_e32 v134, 0xbfb8aa3b, v134
	v_mul_f32_e32 v159, 0xbfb8aa3b, v159
	v_pk_add_f32 v[156:157], v[156:157], 1.0 op_sel_hi:[1,0]
	v_exp_f32_e32 v158, v134
	v_add_f32_e32 v134, 1.0, v178
	v_max_f32_e32 v178, v179, v179
	v_exp_f32_e32 v179, v159
	v_pk_mul_f32 v[156:157], v[162:163], v[156:157]
	v_cvt_pk_f32_fp8_e32 v[180:181], v153
	v_pk_mul_f32 v[70:71], v[70:71], v[156:157]
	v_med3_f32 v156, v160, s35, v177
	v_med3_f32 v178, v178, s35, v177
	v_mul_f32_e32 v156, 0xbfb8aa3b, v156
	v_mul_f32_e32 v159, 0xbfb8aa3b, v178
	v_rcp_f32_e32 v178, v134
	v_add_f32_e32 v134, 1.0, v179
	v_exp_f32_e32 v157, v156
	v_exp_f32_e32 v159, v159
	v_rcp_f32_e32 v179, v134
	v_med3_f32 v134, v180, s35, v177
	v_mul_f32_e32 v134, 0xbfb8aa3b, v134
	v_exp_f32_e32 v156, v134
	v_add_f32_e32 v134, 1.0, v157
	v_pk_add_f32 v[158:159], v[158:159], 1.0 op_sel_hi:[1,0]
	v_med3_f32 v157, v161, s35, v177
	v_pk_mul_f32 v[158:159], v[178:179], v[158:159]
	v_mul_f32_e32 v157, 0xbfb8aa3b, v157
	v_pk_mul_f32 v[72:73], v[72:73], v[158:159]
	v_exp_f32_e32 v159, v157
	v_cvt_pk_f32_fp8_sdwa v[154:155], v155 src0_sel:WORD_1
	v_cvt_pk_f32_fp8_sdwa v[152:153], v153 src0_sel:WORD_1
	v_rcp_f32_e32 v158, v134
	v_med3_f32 v134, v181, s35, v177
	v_mul_f32_e32 v134, 0xbfb8aa3b, v134
	v_exp_f32_e32 v157, v134
	v_add_f32_e32 v134, 1.0, v159
	v_rcp_f32_e32 v159, v134
	v_max_f32_e32 v134, v152, v152
	v_med3_f32 v152, v154, s35, v177
	v_mul_f32_e32 v152, 0xbfb8aa3b, v152
	v_exp_f32_e32 v154, v152
	v_med3_f32 v134, v134, s35, v177
	v_mul_f32_e32 v134, 0xbfb8aa3b, v134
	v_exp_f32_e32 v152, v134
	v_add_f32_e32 v134, 1.0, v154
	v_med3_f32 v154, v155, s35, v177
	v_mul_f32_e32 v154, 0xbfb8aa3b, v154
	v_exp_f32_e32 v155, v154
	v_med3_f32 v153, v153, s35, v177
	v_mul_f32_e32 v153, 0xbfb8aa3b, v153
	v_exp_f32_e32 v153, v153
	v_rcp_f32_e32 v154, v134
	v_add_f32_e32 v134, 1.0, v155
	v_rcp_f32_e32 v155, v134
	v_pk_add_f32 v[152:153], v[152:153], 1.0 op_sel_hi:[1,0]
	v_pk_add_f32 v[156:157], v[156:157], 1.0 op_sel_hi:[1,0]
	v_cvt_pk_f32_fp8_sdwa v[160:161], v148 src0_sel:WORD_1
	v_pk_mul_f32 v[152:153], v[154:155], v[152:153]
	v_pk_mul_f32 v[156:157], v[158:159], v[156:157]
	v_pk_mul_f32 v[60:61], v[60:61], v[152:153]
	v_cvt_pk_f32_fp8_e32 v[152:153], v150
	v_cvt_pk_f32_fp8_e32 v[158:159], v148
	v_cvt_pk_f32_fp8_sdwa v[154:155], v150 src0_sel:WORD_1
	v_pk_mul_f32 v[58:59], v[58:59], v[156:157]
	v_med3_f32 v152, v152, s35, v177
	v_mul_f32_e32 v152, 0xbfb8aa3b, v152
	v_max_f32_e32 v134, v158, v158
	v_exp_f32_e32 v158, v152
	v_med3_f32 v134, v134, s35, v177
	v_mul_f32_e32 v134, 0xbfb8aa3b, v134
	v_med3_f32 v153, v153, s35, v177
	v_exp_f32_e32 v152, v134
	v_add_f32_e32 v134, 1.0, v158
	v_mul_f32_e32 v153, 0xbfb8aa3b, v153
	v_rcp_f32_e32 v158, v134
	v_max_f32_e32 v134, v159, v159
	v_exp_f32_e32 v159, v153
	v_med3_f32 v134, v134, s35, v177
	v_mul_f32_e32 v134, 0xbfb8aa3b, v134
	v_med3_f32 v154, v154, s35, v177
	v_exp_f32_e32 v153, v134
	v_add_f32_e32 v134, 1.0, v159
	v_mul_f32_e32 v154, 0xbfb8aa3b, v154
	v_rcp_f32_e32 v159, v134
	v_max_f32_e32 v134, v160, v160
	v_exp_f32_e32 v160, v154
	v_cvt_pk_f32_fp8_e32 v[156:157], v151
	v_med3_f32 v134, v134, s35, v177
	v_med3_f32 v155, v155, s35, v177
	v_mul_f32_e32 v134, 0xbfb8aa3b, v134
	v_mul_f32_e32 v155, 0xbfb8aa3b, v155
	v_pk_add_f32 v[152:153], v[152:153], 1.0 op_sel_hi:[1,0]
	v_exp_f32_e32 v154, v134
	v_add_f32_e32 v134, 1.0, v160
	v_max_f32_e32 v160, v161, v161
	v_exp_f32_e32 v161, v155
	v_pk_mul_f32 v[152:153], v[158:159], v[152:153]
	v_cvt_pk_f32_fp8_e32 v[162:163], v149
	v_pk_mul_f32 v[46:47], v[46:47], v[152:153]
	v_med3_f32 v152, v156, s35, v177
	v_med3_f32 v160, v160, s35, v177
	v_mul_f32_e32 v152, 0xbfb8aa3b, v152
	v_mul_f32_e32 v155, 0xbfb8aa3b, v160
	v_rcp_f32_e32 v160, v134
	v_add_f32_e32 v134, 1.0, v161
	v_exp_f32_e32 v153, v152
	v_exp_f32_e32 v155, v155
	v_rcp_f32_e32 v161, v134
	v_med3_f32 v134, v162, s35, v177
	v_mul_f32_e32 v134, 0xbfb8aa3b, v134
	v_exp_f32_e32 v152, v134
	v_add_f32_e32 v134, 1.0, v153
	v_pk_add_f32 v[154:155], v[154:155], 1.0 op_sel_hi:[1,0]
	v_med3_f32 v153, v157, s35, v177
	v_pk_mul_f32 v[154:155], v[160:161], v[154:155]
	v_mul_f32_e32 v153, 0xbfb8aa3b, v153
	v_pk_mul_f32 v[48:49], v[48:49], v[154:155]
	v_exp_f32_e32 v155, v153
	v_cvt_pk_f32_fp8_sdwa v[150:151], v151 src0_sel:WORD_1
	v_cvt_pk_f32_fp8_sdwa v[148:149], v149 src0_sel:WORD_1
	v_rcp_f32_e32 v154, v134
	v_med3_f32 v134, v163, s35, v177
	v_mul_f32_e32 v134, 0xbfb8aa3b, v134
	v_exp_f32_e32 v153, v134
	v_add_f32_e32 v134, 1.0, v155
	v_rcp_f32_e32 v155, v134
	v_max_f32_e32 v134, v148, v148
	v_med3_f32 v148, v150, s35, v177
	v_mul_f32_e32 v148, 0xbfb8aa3b, v148
	v_exp_f32_e32 v150, v148
	v_med3_f32 v134, v134, s35, v177
	v_mul_f32_e32 v134, 0xbfb8aa3b, v134
	v_exp_f32_e32 v148, v134
	v_add_f32_e32 v134, 1.0, v150
	v_med3_f32 v150, v151, s35, v177
	v_mul_f32_e32 v150, 0xbfb8aa3b, v150
	v_exp_f32_e32 v151, v150
	v_med3_f32 v149, v149, s35, v177
	v_mul_f32_e32 v149, 0xbfb8aa3b, v149
	v_exp_f32_e32 v149, v149
	v_rcp_f32_e32 v150, v134
	v_add_f32_e32 v134, 1.0, v151
	v_rcp_f32_e32 v151, v134
	v_pk_add_f32 v[148:149], v[148:149], 1.0 op_sel_hi:[1,0]
	v_pk_add_f32 v[152:153], v[152:153], 1.0 op_sel_hi:[1,0]
	v_cvt_pk_f32_fp8_sdwa v[156:157], v144 src0_sel:WORD_1
	v_pk_mul_f32 v[148:149], v[150:151], v[148:149]
	v_pk_mul_f32 v[152:153], v[154:155], v[152:153]
	v_pk_mul_f32 v[36:37], v[36:37], v[148:149]
	v_cvt_pk_f32_fp8_e32 v[148:149], v146
	v_cvt_pk_f32_fp8_e32 v[154:155], v144
	v_cvt_pk_f32_fp8_sdwa v[150:151], v146 src0_sel:WORD_1
	v_pk_mul_f32 v[34:35], v[34:35], v[152:153]
	v_med3_f32 v148, v148, s35, v177
	v_mul_f32_e32 v148, 0xbfb8aa3b, v148
	v_max_f32_e32 v134, v154, v154
	v_exp_f32_e32 v154, v148
	v_med3_f32 v134, v134, s35, v177
	v_mul_f32_e32 v134, 0xbfb8aa3b, v134
	v_med3_f32 v149, v149, s35, v177
	v_exp_f32_e32 v148, v134
	v_add_f32_e32 v134, 1.0, v154
	v_mul_f32_e32 v149, 0xbfb8aa3b, v149
	v_rcp_f32_e32 v154, v134
	v_max_f32_e32 v134, v155, v155
	v_exp_f32_e32 v155, v149
	v_med3_f32 v134, v134, s35, v177
	v_mul_f32_e32 v134, 0xbfb8aa3b, v134
	v_med3_f32 v150, v150, s35, v177
	v_exp_f32_e32 v149, v134
	v_add_f32_e32 v134, 1.0, v155
	v_mul_f32_e32 v150, 0xbfb8aa3b, v150
	v_rcp_f32_e32 v155, v134
	v_max_f32_e32 v134, v156, v156
	v_exp_f32_e32 v156, v150
	v_cvt_pk_f32_fp8_e32 v[152:153], v147
	v_med3_f32 v134, v134, s35, v177
	v_med3_f32 v151, v151, s35, v177
	v_mul_f32_e32 v134, 0xbfb8aa3b, v134
	v_mul_f32_e32 v151, 0xbfb8aa3b, v151
	v_pk_add_f32 v[148:149], v[148:149], 1.0 op_sel_hi:[1,0]
	v_exp_f32_e32 v150, v134
	v_add_f32_e32 v134, 1.0, v156
	v_max_f32_e32 v156, v157, v157
	v_exp_f32_e32 v157, v151
	v_pk_mul_f32 v[148:149], v[154:155], v[148:149]
	v_cvt_pk_f32_fp8_e32 v[158:159], v145
	v_pk_mul_f32 v[22:23], v[22:23], v[148:149]
	v_med3_f32 v148, v152, s35, v177
	v_med3_f32 v156, v156, s35, v177
	v_mul_f32_e32 v148, 0xbfb8aa3b, v148
	v_mul_f32_e32 v151, 0xbfb8aa3b, v156
	v_rcp_f32_e32 v156, v134
	v_add_f32_e32 v134, 1.0, v157
	v_exp_f32_e32 v149, v148
	v_exp_f32_e32 v151, v151
	v_rcp_f32_e32 v157, v134
	v_med3_f32 v134, v158, s35, v177
	v_mul_f32_e32 v134, 0xbfb8aa3b, v134
	v_exp_f32_e32 v148, v134
	v_add_f32_e32 v134, 1.0, v149
	v_pk_add_f32 v[150:151], v[150:151], 1.0 op_sel_hi:[1,0]
	v_med3_f32 v149, v153, s35, v177
	v_pk_mul_f32 v[150:151], v[156:157], v[150:151]
	v_mul_f32_e32 v149, 0xbfb8aa3b, v149
	v_pk_mul_f32 v[24:25], v[24:25], v[150:151]
	v_exp_f32_e32 v151, v149
	v_cvt_pk_f32_fp8_sdwa v[146:147], v147 src0_sel:WORD_1
	v_cvt_pk_f32_fp8_sdwa v[144:145], v145 src0_sel:WORD_1
	v_rcp_f32_e32 v150, v134
	v_med3_f32 v134, v159, s35, v177
	v_mul_f32_e32 v134, 0xbfb8aa3b, v134
	v_exp_f32_e32 v149, v134
	v_add_f32_e32 v134, 1.0, v151
	v_rcp_f32_e32 v151, v134
	v_max_f32_e32 v134, v144, v144
	v_med3_f32 v144, v146, s35, v177
	v_mul_f32_e32 v144, 0xbfb8aa3b, v144
	v_exp_f32_e32 v146, v144
	v_med3_f32 v134, v134, s35, v177
	v_mul_f32_e32 v134, 0xbfb8aa3b, v134
	v_exp_f32_e32 v144, v134
	v_add_f32_e32 v134, 1.0, v146
	v_med3_f32 v146, v147, s35, v177
	v_mul_f32_e32 v146, 0xbfb8aa3b, v146
	v_exp_f32_e32 v147, v146
	v_med3_f32 v145, v145, s35, v177
	v_mul_f32_e32 v145, 0xbfb8aa3b, v145
	v_exp_f32_e32 v145, v145
	v_rcp_f32_e32 v146, v134
	v_add_f32_e32 v134, 1.0, v147
	v_rcp_f32_e32 v147, v134
	v_pk_add_f32 v[144:145], v[144:145], 1.0 op_sel_hi:[1,0]
	v_pk_add_f32 v[148:149], v[148:149], 1.0 op_sel_hi:[1,0]
	v_cvt_pk_f32_fp8_sdwa v[152:153], v140 src0_sel:WORD_1
	v_pk_mul_f32 v[144:145], v[146:147], v[144:145]
	v_pk_mul_f32 v[148:149], v[150:151], v[148:149]
	v_pk_mul_f32 v[20:21], v[20:21], v[144:145]
	v_cvt_pk_f32_fp8_e32 v[144:145], v142
	v_cvt_pk_f32_fp8_e32 v[150:151], v140
	v_cvt_pk_f32_fp8_sdwa v[146:147], v142 src0_sel:WORD_1
	v_pk_mul_f32 v[18:19], v[18:19], v[148:149]
	v_med3_f32 v144, v144, s35, v177
	v_mul_f32_e32 v144, 0xbfb8aa3b, v144
	v_max_f32_e32 v134, v150, v150
	v_exp_f32_e32 v150, v144
	v_med3_f32 v134, v134, s35, v177
	v_mul_f32_e32 v134, 0xbfb8aa3b, v134
	v_med3_f32 v145, v145, s35, v177
	v_exp_f32_e32 v144, v134
	v_add_f32_e32 v134, 1.0, v150
	v_mul_f32_e32 v145, 0xbfb8aa3b, v145
	v_rcp_f32_e32 v150, v134
	v_max_f32_e32 v134, v151, v151
	v_exp_f32_e32 v151, v145
	v_med3_f32 v134, v134, s35, v177
	v_mul_f32_e32 v134, 0xbfb8aa3b, v134
	v_med3_f32 v146, v146, s35, v177
	v_exp_f32_e32 v145, v134
	v_add_f32_e32 v134, 1.0, v151
	v_mul_f32_e32 v146, 0xbfb8aa3b, v146
	v_rcp_f32_e32 v151, v134
	v_max_f32_e32 v134, v152, v152
	v_exp_f32_e32 v152, v146
	v_cvt_pk_f32_fp8_e32 v[148:149], v143
	v_med3_f32 v134, v134, s35, v177
	v_med3_f32 v147, v147, s35, v177
	v_mul_f32_e32 v134, 0xbfb8aa3b, v134
	v_mul_f32_e32 v147, 0xbfb8aa3b, v147
	v_pk_add_f32 v[144:145], v[144:145], 1.0 op_sel_hi:[1,0]
	v_exp_f32_e32 v146, v134
	v_add_f32_e32 v134, 1.0, v152
	v_max_f32_e32 v152, v153, v153
	v_exp_f32_e32 v153, v147
	v_pk_mul_f32 v[144:145], v[150:151], v[144:145]
	v_cvt_pk_f32_fp8_e32 v[154:155], v141
	v_pk_mul_f32 v[14:15], v[14:15], v[144:145]
	v_med3_f32 v144, v148, s35, v177
	v_med3_f32 v152, v152, s35, v177
	v_mul_f32_e32 v144, 0xbfb8aa3b, v144
	v_mul_f32_e32 v147, 0xbfb8aa3b, v152
	v_rcp_f32_e32 v152, v134
	v_add_f32_e32 v134, 1.0, v153
	v_exp_f32_e32 v145, v144
	v_exp_f32_e32 v147, v147
	v_rcp_f32_e32 v153, v134
	v_med3_f32 v134, v154, s35, v177
	v_mul_f32_e32 v134, 0xbfb8aa3b, v134
	v_exp_f32_e32 v144, v134
	v_add_f32_e32 v134, 1.0, v145
	v_pk_add_f32 v[146:147], v[146:147], 1.0 op_sel_hi:[1,0]
	v_med3_f32 v145, v149, s35, v177
	v_pk_mul_f32 v[146:147], v[152:153], v[146:147]
	v_mul_f32_e32 v145, 0xbfb8aa3b, v145
	v_pk_mul_f32 v[16:17], v[16:17], v[146:147]
	v_exp_f32_e32 v147, v145
	v_cvt_pk_f32_fp8_sdwa v[142:143], v143 src0_sel:WORD_1
	v_cvt_pk_f32_fp8_sdwa v[140:141], v141 src0_sel:WORD_1
	v_rcp_f32_e32 v146, v134
	v_med3_f32 v134, v155, s35, v177
	v_mul_f32_e32 v134, 0xbfb8aa3b, v134
	v_exp_f32_e32 v145, v134
	v_add_f32_e32 v134, 1.0, v147
	v_rcp_f32_e32 v147, v134
	v_max_f32_e32 v134, v140, v140
	v_med3_f32 v140, v142, s35, v177
	v_mul_f32_e32 v140, 0xbfb8aa3b, v140
	v_exp_f32_e32 v142, v140
	v_med3_f32 v134, v134, s35, v177
	v_mul_f32_e32 v134, 0xbfb8aa3b, v134
	v_exp_f32_e32 v140, v134
	v_add_f32_e32 v134, 1.0, v142
	v_med3_f32 v142, v143, s35, v177
	v_mul_f32_e32 v142, 0xbfb8aa3b, v142
	v_exp_f32_e32 v143, v142
	v_med3_f32 v141, v141, s35, v177
	v_mul_f32_e32 v141, 0xbfb8aa3b, v141
	v_exp_f32_e32 v141, v141
	v_rcp_f32_e32 v142, v134
	v_add_f32_e32 v134, 1.0, v143
	v_rcp_f32_e32 v143, v134
	v_pk_add_f32 v[140:141], v[140:141], 1.0 op_sel_hi:[1,0]
	v_pk_add_f32 v[144:145], v[144:145], 1.0 op_sel_hi:[1,0]
	s_waitcnt vmcnt(0)
	v_cvt_pk_f32_fp8_sdwa v[148:149], v136 src0_sel:WORD_1
	v_pk_mul_f32 v[140:141], v[142:143], v[140:141]
	v_pk_mul_f32 v[144:145], v[146:147], v[144:145]
	v_pk_mul_f32 v[12:13], v[12:13], v[140:141]
	v_cvt_pk_f32_fp8_e32 v[140:141], v138
	v_cvt_pk_f32_fp8_e32 v[146:147], v136
	v_cvt_pk_f32_fp8_sdwa v[142:143], v138 src0_sel:WORD_1
	v_pk_mul_f32 v[10:11], v[10:11], v[144:145]
	v_med3_f32 v140, v140, s35, v177
	v_mul_f32_e32 v140, 0xbfb8aa3b, v140
	v_max_f32_e32 v134, v146, v146
	v_exp_f32_e32 v146, v140
	v_med3_f32 v134, v134, s35, v177
	v_mul_f32_e32 v134, 0xbfb8aa3b, v134
	v_med3_f32 v141, v141, s35, v177
	v_exp_f32_e32 v140, v134
	v_add_f32_e32 v134, 1.0, v146
	v_mul_f32_e32 v141, 0xbfb8aa3b, v141
	v_rcp_f32_e32 v146, v134
	v_max_f32_e32 v134, v147, v147
	v_exp_f32_e32 v147, v141
	v_med3_f32 v134, v134, s35, v177
	v_mul_f32_e32 v134, 0xbfb8aa3b, v134
	v_med3_f32 v142, v142, s35, v177
	v_exp_f32_e32 v141, v134
	v_add_f32_e32 v134, 1.0, v147
	v_mul_f32_e32 v142, 0xbfb8aa3b, v142
	v_rcp_f32_e32 v147, v134
	v_max_f32_e32 v134, v148, v148
	v_exp_f32_e32 v148, v142
	v_cvt_pk_f32_fp8_e32 v[144:145], v139
	v_med3_f32 v134, v134, s35, v177
	v_med3_f32 v143, v143, s35, v177
	v_mul_f32_e32 v134, 0xbfb8aa3b, v134
	v_mul_f32_e32 v143, 0xbfb8aa3b, v143
	v_pk_add_f32 v[140:141], v[140:141], 1.0 op_sel_hi:[1,0]
	v_exp_f32_e32 v142, v134
	v_add_f32_e32 v134, 1.0, v148
	v_max_f32_e32 v148, v149, v149
	v_exp_f32_e32 v149, v143
	v_pk_mul_f32 v[140:141], v[146:147], v[140:141]
	v_cvt_pk_f32_fp8_e32 v[150:151], v137
	v_pk_mul_f32 v[6:7], v[6:7], v[140:141]
	v_med3_f32 v140, v144, s35, v177
	v_med3_f32 v148, v148, s35, v177
	v_mul_f32_e32 v140, 0xbfb8aa3b, v140
	v_mul_f32_e32 v143, 0xbfb8aa3b, v148
	v_rcp_f32_e32 v148, v134
	v_add_f32_e32 v134, 1.0, v149
	v_exp_f32_e32 v141, v140
	v_exp_f32_e32 v143, v143
	v_rcp_f32_e32 v149, v134
	v_med3_f32 v134, v150, s35, v177
	v_mul_f32_e32 v134, 0xbfb8aa3b, v134
	v_exp_f32_e32 v140, v134
	v_add_f32_e32 v134, 1.0, v141
	v_pk_add_f32 v[142:143], v[142:143], 1.0 op_sel_hi:[1,0]
	v_med3_f32 v141, v145, s35, v177
	v_pk_mul_f32 v[142:143], v[148:149], v[142:143]
	v_mul_f32_e32 v141, 0xbfb8aa3b, v141
	v_pk_mul_f32 v[8:9], v[8:9], v[142:143]
	v_exp_f32_e32 v143, v141
	v_cvt_pk_f32_fp8_sdwa v[138:139], v139 src0_sel:WORD_1
	v_cvt_pk_f32_fp8_sdwa v[136:137], v137 src0_sel:WORD_1
	v_rcp_f32_e32 v142, v134
	v_med3_f32 v134, v151, s35, v177
	v_mul_f32_e32 v134, 0xbfb8aa3b, v134
	v_exp_f32_e32 v141, v134
	v_add_f32_e32 v134, 1.0, v143
	v_rcp_f32_e32 v143, v134
	v_max_f32_e32 v134, v136, v136
	v_med3_f32 v136, v138, s35, v177
	v_mul_f32_e32 v136, 0xbfb8aa3b, v136
	v_exp_f32_e32 v138, v136
	v_med3_f32 v134, v134, s35, v177
	v_mul_f32_e32 v134, 0xbfb8aa3b, v134
	v_exp_f32_e32 v136, v134
	v_add_f32_e32 v134, 1.0, v138
	v_med3_f32 v138, v139, s35, v177
	v_mul_f32_e32 v138, 0xbfb8aa3b, v138
	v_exp_f32_e32 v139, v138
	v_med3_f32 v137, v137, s35, v177
	v_mul_f32_e32 v137, 0xbfb8aa3b, v137
	v_exp_f32_e32 v137, v137
	v_rcp_f32_e32 v138, v134
	v_add_f32_e32 v134, 1.0, v139
	v_rcp_f32_e32 v139, v134
	v_pk_add_f32 v[136:137], v[136:137], 1.0 op_sel_hi:[1,0]
	v_pk_add_f32 v[140:141], v[140:141], 1.0 op_sel_hi:[1,0]
	v_pk_mul_f32 v[136:137], v[138:139], v[136:137]
	v_pk_mul_f32 v[140:141], v[142:143], v[140:141]
	v_pk_mul_f32 v[4:5], v[4:5], v[136:137]
	v_pk_mul_f32 v[2:3], v[2:3], v[140:141]
	s_nop 0

.LBB0_1051:
	v_mov_b32_e32 v134, v170
	v_mov_b32_e32 v136, v169
	s_lshl_b32 s2, s60, 8
	s_add_i32 s2, s2, s87
	v_add_lshl_u32 v136, s2, v136, 10
	s_or_b32 s2, s23, s91
	v_lshlrev_b32_e32 v134, 3, v134
	v_add3_u32 v134, s2, v134, v136
	s_lshl_b32 s32, s23, 8
	v_add_u32_e32 v216, s32, v214
	s_lshl_b32 s32, s60, 18
	v_add_u32_e32 v216, s32, v216
	v_add_u32_e32 v217, 0x1000, v216
	v_mov_b64_e32 v[178:179], v[220:221]
	v_mov_b64_e32 v[182:183], v[224:225]
	v_lshl_add_u64 v[136:137], s[16:17], 0, v[134:135]
	v_add_co_u32_e32 v138, vcc, 0x4000, v136
	s_mov_b32 s2, 0x8000
	s_nop 0
	v_addc_co_u32_e32 v139, vcc, 0, v137, vcc
	v_add_co_u32_e32 v140, vcc, 0x8000, v136
	s_waitcnt vmcnt(1)
	v_cvt_pk_f32_fp8_e32 v[180:181], v178
	v_addc_co_u32_e32 v141, vcc, 0, v137, vcc
	v_mov_b64_e32 v[162:163], v[228:229]
	v_mov_b64_e32 v[160:161], v[232:233]
	v_mov_b64_e32 v[158:159], v[236:237]
	v_mov_b64_e32 v[156:157], v[240:241]
	v_cvt_pk_f32_fp8_sdwa v[184:185], v178 src0_sel:WORD_1
	v_cvt_pk_f32_fp8_e32 v[186:187], v179
	v_cvt_pk_f32_fp8_sdwa v[178:179], v179 src0_sel:WORD_1
	v_med3_f32 v180, v180, s35, v177
	v_med3_f32 v181, v181, s35, v177
	v_med3_f32 v184, v184, s35, v177
	v_med3_f32 v185, v185, s35, v177
	v_mul_f32_e32 v180, 0xbfb8aa3b, v180
	v_mul_f32_e32 v181, 0xbfb8aa3b, v181
	v_mul_f32_e32 v184, 0xbfb8aa3b, v184
	v_mul_f32_e32 v185, 0xbfb8aa3b, v185
	v_exp_f32_e32 v180, v180
	v_exp_f32_e32 v181, v181
	v_exp_f32_e32 v184, v184
	v_exp_f32_e32 v185, v185
	v_med3_f32 v178, v178, s35, v177
	v_mul_f32_e32 v178, 0xbfb8aa3b, v178
	v_med3_f32 v179, v179, s35, v177
	v_med3_f32 v186, v186, s35, v177
	v_med3_f32 v187, v187, s35, v177
	v_add_f32_e32 v180, 1.0, v180
	v_add_f32_e32 v181, 1.0, v181
	v_exp_f32_e32 v178, v178
	v_mul_f32_e32 v179, 0xbfb8aa3b, v179
	v_mul_f32_e32 v186, 0xbfb8aa3b, v186
	v_mul_f32_e32 v187, 0xbfb8aa3b, v187
	v_add_f32_e32 v184, 1.0, v184
	v_add_f32_e32 v185, 1.0, v185
	v_rcp_f32_e32 v180, v180
	v_rcp_f32_e32 v181, v181
	v_exp_f32_e32 v179, v179
	v_exp_f32_e32 v186, v186
	v_exp_f32_e32 v187, v187
	v_rcp_f32_e32 v184, v184
	v_rcp_f32_e32 v185, v185
	v_add_f32_e32 v178, 1.0, v178
	v_rcp_f32_e32 v188, v178
	v_add_f32_e32 v178, 1.0, v179
	v_pk_mul_f32 v[26:27], v[26:27], v[180:181]
	v_add_co_u32_e32 v142, vcc, 0xc000, v136
	v_add_f32_e32 v186, 1.0, v186
	v_add_f32_e32 v187, 1.0, v187
	v_rcp_f32_e32 v189, v178
	v_cvt_pk_bf16_f32 v178, v26, v27
	v_pk_mul_f32 v[26:27], v[28:29], v[184:185]
	s_waitcnt vmcnt(4)
	v_cvt_pk_f32_fp8_e32 v[28:29], v182
	v_addc_co_u32_e32 v143, vcc, 0, v137, vcc
	v_rcp_f32_e32 v186, v186
	v_rcp_f32_e32 v187, v187
	v_add_co_u32_e32 v138, vcc, 0x20000, v136
	s_nop 0
	v_addc_co_u32_e32 v139, vcc, 0, v137, vcc
	v_add_co_u32_e32 v140, vcc, 0x24000, v136
	v_cvt_pk_bf16_f32 v179, v26, v27
	s_nop 0
	v_addc_co_u32_e32 v141, vcc, 0, v137, vcc
	v_pk_mul_f32 v[26:27], v[30:31], v[186:187]
	v_med3_f32 v28, v28, s35, v177
	v_mov_b64_e32 v[154:155], v[244:245]
	v_mov_b64_e32 v[152:153], v[248:249]
	v_mov_b64_e32 v[150:151], v[222:223]
	v_mov_b64_e32 v[148:149], v[226:227]
	v_add_co_u32_e32 v138, vcc, 0x28000, v136
	v_cvt_pk_bf16_f32 v180, v26, v27
	v_pk_mul_f32 v[26:27], v[32:33], v[188:189]
	v_mul_f32_e32 v28, 0xbfb8aa3b, v28
	v_addc_co_u32_e32 v139, vcc, 0, v137, vcc
	v_cvt_pk_bf16_f32 v181, v26, v27
	v_lshl_add_u64 v[26:27], v[134:135], 1, s[18:19]
	v_exp_f32_e32 v134, v28
	v_add_co_u32_e32 v136, vcc, 0x2c000, v136
	v_med3_f32 v28, v29, s35, v177
	s_nop 0
	v_addc_co_u32_e32 v137, vcc, 0, v137, vcc
	v_mul_f32_e32 v28, 0xbfb8aa3b, v28
	v_mov_b64_e32 v[146:147], v[230:231]
	v_mov_b64_e32 v[144:145], v[234:235]
	v_mov_b64_e32 v[142:143], v[238:239]
	s_nop 0
	v_mov_b64_e32 v[140:141], v[242:243]
	s_nop 0
	v_mov_b64_e32 v[138:139], v[246:247]
	s_nop 0
	v_mov_b64_e32 v[136:137], v[250:251]
	v_cvt_pk_f32_fp8_sdwa v[30:31], v182 src0_sel:WORD_1
	global_store_dwordx4 v[26:27], v[178:181], off
	v_cvt_pk_f32_fp8_e32 v[32:33], v183
	v_add_f32_e32 v134, 1.0, v134
	v_exp_f32_e32 v179, v28
	v_cvt_pk_f32_fp8_sdwa v[28:29], v183 src0_sel:WORD_1
	v_med3_f32 v30, v30, s35, v177
	v_med3_f32 v31, v31, s35, v177
	v_med3_f32 v28, v28, s35, v177
	v_mul_f32_e32 v30, 0xbfb8aa3b, v30
	v_mul_f32_e32 v31, 0xbfb8aa3b, v31
	v_med3_f32 v32, v32, s35, v177
	v_med3_f32 v33, v33, s35, v177
	v_mul_f32_e32 v28, 0xbfb8aa3b, v28
	v_med3_f32 v29, v29, s35, v177
	v_exp_f32_e32 v30, v30
	v_exp_f32_e32 v31, v31
	v_mul_f32_e32 v32, 0xbfb8aa3b, v32
	v_mul_f32_e32 v33, 0xbfb8aa3b, v33
	v_exp_f32_e32 v28, v28
	v_mul_f32_e32 v29, 0xbfb8aa3b, v29
	v_exp_f32_e32 v32, v32
	v_exp_f32_e32 v33, v33
	v_exp_f32_e32 v29, v29
	v_rcp_f32_e32 v178, v134
	v_add_f32_e32 v134, 1.0, v179
	v_add_f32_e32 v30, 1.0, v30
	v_add_f32_e32 v31, 1.0, v31
	v_add_f32_e32 v28, 1.0, v28
	v_rcp_f32_e32 v179, v134
	v_rcp_f32_e32 v30, v30
	v_rcp_f32_e32 v31, v31
	v_add_f32_e32 v32, 1.0, v32
	v_add_f32_e32 v33, 1.0, v33
	v_rcp_f32_e32 v180, v28
	v_add_f32_e32 v28, 1.0, v29
	v_rcp_f32_e32 v32, v32
	v_rcp_f32_e32 v33, v33
	v_rcp_f32_e32 v181, v28
	v_pk_mul_f32 v[28:29], v[38:39], v[178:179]
	v_pk_mul_f32 v[30:31], v[40:41], v[30:31]
	v_cvt_pk_bf16_f32 v28, v28, v29
	v_cvt_pk_bf16_f32 v29, v30, v31
	v_pk_mul_f32 v[30:31], v[42:43], v[32:33]
	v_pk_mul_f32 v[32:33], v[44:45], v[180:181]
	v_cvt_pk_bf16_f32 v30, v30, v31
	v_cvt_pk_bf16_f32 v31, v32, v33
	global_store_dwordx4 v[26:27], v[28:31], off offset:256
	s_waitcnt vmcnt(15)
	v_cvt_pk_f32_fp8_e32 v[32:33], v162
	v_cvt_pk_f32_fp8_sdwa v[28:29], v162 src0_sel:WORD_1
	v_cvt_pk_f32_fp8_e32 v[30:31], v163
	v_med3_f32 v32, v32, s35, v177
	v_mul_f32_e32 v32, 0xbfb8aa3b, v32
	v_med3_f32 v28, v28, s35, v177
	v_mul_f32_e32 v28, 0xbfb8aa3b, v28
	v_med3_f32 v29, v29, s35, v177
	v_exp_f32_e32 v28, v28
	v_mul_f32_e32 v29, 0xbfb8aa3b, v29
	v_exp_f32_e32 v29, v29
	v_exp_f32_e32 v38, v32
	v_add_f32_e32 v28, 1.0, v28
	v_rcp_f32_e32 v40, v28
	v_add_f32_e32 v28, 1.0, v29
	v_med3_f32 v32, v33, s35, v177
	v_med3_f32 v29, v30, s35, v177
	v_mul_f32_e32 v32, 0xbfb8aa3b, v32
	v_mul_f32_e32 v29, 0xbfb8aa3b, v29
	v_med3_f32 v30, v31, s35, v177
	v_exp_f32_e32 v39, v32
	v_cvt_pk_f32_fp8_sdwa v[32:33], v163 src0_sel:WORD_1
	v_exp_f32_e32 v29, v29
	v_mul_f32_e32 v30, 0xbfb8aa3b, v30
	v_exp_f32_e32 v31, v30
	v_rcp_f32_e32 v41, v28
	v_add_f32_e32 v28, 1.0, v29
	v_rcp_f32_e32 v30, v28
	v_add_f32_e32 v28, 1.0, v31
	v_med3_f32 v29, v32, s35, v177
	v_mul_f32_e32 v29, 0xbfb8aa3b, v29
	v_med3_f32 v31, v33, s35, v177
	v_exp_f32_e32 v29, v29
	v_mul_f32_e32 v31, 0xbfb8aa3b, v31
	v_exp_f32_e32 v33, v31
	v_rcp_f32_e32 v31, v28
	v_add_f32_e32 v28, 1.0, v29
	v_rcp_f32_e32 v32, v28
	v_add_f32_e32 v28, 1.0, v33
	v_add_f32_e32 v38, 1.0, v38
	v_add_f32_e32 v39, 1.0, v39
	v_rcp_f32_e32 v33, v28
	v_rcp_f32_e32 v38, v38
	v_rcp_f32_e32 v39, v39
	v_pk_mul_f32 v[30:31], v[54:55], v[30:31]
	v_pk_mul_f32 v[32:33], v[56:57], v[32:33]
	v_cvt_pk_bf16_f32 v30, v30, v31
	v_pk_mul_f32 v[28:29], v[50:51], v[38:39]
	v_pk_mul_f32 v[38:39], v[52:53], v[40:41]
	v_cvt_pk_bf16_f32 v31, v32, v33
	v_add_co_u32_e32 v32, vcc, s2, v26
	v_cvt_pk_bf16_f32 v28, v28, v29
	v_cvt_pk_bf16_f32 v29, v38, v39
	v_addc_co_u32_e32 v33, vcc, 0, v27, vcc
	global_store_dwordx4 v[32:33], v[28:31], off
	s_waitcnt vmcnt(15)
	v_cvt_pk_f32_fp8_e32 v[38:39], v160
	s_mov_b32 s2, 0x10000
	v_cvt_pk_f32_fp8_sdwa v[28:29], v160 src0_sel:WORD_1
	v_cvt_pk_f32_fp8_e32 v[30:31], v161
	v_med3_f32 v38, v38, s35, v177
	v_med3_f32 v28, v28, s35, v177
	v_mul_f32_e32 v28, 0xbfb8aa3b, v28
	v_med3_f32 v29, v29, s35, v177
	v_exp_f32_e32 v28, v28
	v_mul_f32_e32 v29, 0xbfb8aa3b, v29
	v_exp_f32_e32 v29, v29
	v_mul_f32_e32 v38, 0xbfb8aa3b, v38
	v_add_f32_e32 v28, 1.0, v28
	v_exp_f32_e32 v40, v38
	v_rcp_f32_e32 v42, v28
	v_add_f32_e32 v28, 1.0, v29
	v_med3_f32 v38, v39, s35, v177
	v_med3_f32 v29, v30, s35, v177
	v_mul_f32_e32 v38, 0xbfb8aa3b, v38
	v_mul_f32_e32 v29, 0xbfb8aa3b, v29
	v_med3_f32 v30, v31, s35, v177
	v_exp_f32_e32 v41, v38
	v_cvt_pk_f32_fp8_sdwa v[38:39], v161 src0_sel:WORD_1
	v_exp_f32_e32 v29, v29
	v_mul_f32_e32 v30, 0xbfb8aa3b, v30
	v_exp_f32_e32 v31, v30
	v_rcp_f32_e32 v43, v28
	v_add_f32_e32 v28, 1.0, v29
	v_rcp_f32_e32 v30, v28
	v_add_f32_e32 v28, 1.0, v31
	v_med3_f32 v29, v38, s35, v177
	v_mul_f32_e32 v29, 0xbfb8aa3b, v29
	v_med3_f32 v31, v39, s35, v177
	v_exp_f32_e32 v29, v29
	v_mul_f32_e32 v31, 0xbfb8aa3b, v31
	v_exp_f32_e32 v39, v31
	v_rcp_f32_e32 v31, v28
	v_add_f32_e32 v28, 1.0, v29
	v_add_f32_e32 v40, 1.0, v40
	v_add_f32_e32 v41, 1.0, v41
	v_rcp_f32_e32 v38, v28
	v_add_f32_e32 v28, 1.0, v39
	v_rcp_f32_e32 v40, v40
	v_rcp_f32_e32 v41, v41
	v_rcp_f32_e32 v39, v28
	v_pk_mul_f32 v[30:31], v[66:67], v[30:31]
	v_pk_mul_f32 v[28:29], v[62:63], v[40:41]
	v_pk_mul_f32 v[40:41], v[64:65], v[42:43]
	v_pk_mul_f32 v[38:39], v[68:69], v[38:39]
	v_cvt_pk_bf16_f32 v28, v28, v29
	v_cvt_pk_bf16_f32 v29, v40, v41
	v_cvt_pk_bf16_f32 v30, v30, v31
	v_cvt_pk_bf16_f32 v31, v38, v39
	global_store_dwordx4 v[32:33], v[28:31], off offset:256
	s_waitcnt vmcnt(15)
	v_cvt_pk_f32_fp8_e32 v[38:39], v158
	v_cvt_pk_f32_fp8_sdwa v[28:29], v158 src0_sel:WORD_1
	v_cvt_pk_f32_fp8_e32 v[30:31], v159
	v_med3_f32 v32, v38, s35, v177
	v_mul_f32_e32 v32, 0xbfb8aa3b, v32
	v_med3_f32 v28, v28, s35, v177
	v_mul_f32_e32 v28, 0xbfb8aa3b, v28
	v_med3_f32 v29, v29, s35, v177
	v_exp_f32_e32 v28, v28
	v_mul_f32_e32 v29, 0xbfb8aa3b, v29
	v_exp_f32_e32 v29, v29
	v_exp_f32_e32 v38, v32
	v_add_f32_e32 v28, 1.0, v28
	v_rcp_f32_e32 v40, v28
	v_add_f32_e32 v28, 1.0, v29
	v_med3_f32 v32, v39, s35, v177
	v_med3_f32 v29, v30, s35, v177
	v_mul_f32_e32 v32, 0xbfb8aa3b, v32
	v_mul_f32_e32 v29, 0xbfb8aa3b, v29
	v_med3_f32 v30, v31, s35, v177
	v_exp_f32_e32 v39, v32
	v_cvt_pk_f32_fp8_sdwa v[32:33], v159 src0_sel:WORD_1
	v_exp_f32_e32 v29, v29
	v_mul_f32_e32 v30, 0xbfb8aa3b, v30
	v_exp_f32_e32 v31, v30
	v_rcp_f32_e32 v41, v28
	v_add_f32_e32 v28, 1.0, v29
	v_rcp_f32_e32 v30, v28
	v_add_f32_e32 v28, 1.0, v31
	v_med3_f32 v29, v32, s35, v177
	v_mul_f32_e32 v29, 0xbfb8aa3b, v29
	v_med3_f32 v31, v33, s35, v177
	v_exp_f32_e32 v29, v29
	v_mul_f32_e32 v31, 0xbfb8aa3b, v31
	v_exp_f32_e32 v33, v31
	v_rcp_f32_e32 v31, v28
	v_add_f32_e32 v28, 1.0, v29
	v_rcp_f32_e32 v32, v28
	v_add_f32_e32 v28, 1.0, v33
	v_add_f32_e32 v38, 1.0, v38
	v_add_f32_e32 v39, 1.0, v39
	v_rcp_f32_e32 v33, v28
	v_rcp_f32_e32 v38, v38
	v_rcp_f32_e32 v39, v39
	v_pk_mul_f32 v[30:31], v[78:79], v[30:31]
	v_pk_mul_f32 v[32:33], v[80:81], v[32:33]
	v_cvt_pk_bf16_f32 v30, v30, v31
	v_pk_mul_f32 v[28:29], v[74:75], v[38:39]
	v_pk_mul_f32 v[38:39], v[76:77], v[40:41]
	v_cvt_pk_bf16_f32 v31, v32, v33
	v_add_co_u32_e32 v32, vcc, s2, v26
	v_cvt_pk_bf16_f32 v28, v28, v29
	v_cvt_pk_bf16_f32 v29, v38, v39
	v_addc_co_u32_e32 v33, vcc, 0, v27, vcc
	global_store_dwordx4 v[32:33], v[28:31], off
	s_waitcnt vmcnt(15)
	v_cvt_pk_f32_fp8_e32 v[38:39], v156
	s_mov_b32 s2, 0x18000
	v_cvt_pk_f32_fp8_sdwa v[28:29], v156 src0_sel:WORD_1
	v_cvt_pk_f32_fp8_e32 v[30:31], v157
	v_med3_f32 v38, v38, s35, v177
	v_med3_f32 v28, v28, s35, v177
	v_mul_f32_e32 v28, 0xbfb8aa3b, v28
	v_med3_f32 v29, v29, s35, v177
	v_exp_f32_e32 v28, v28
	v_mul_f32_e32 v29, 0xbfb8aa3b, v29
	v_exp_f32_e32 v29, v29
	v_mul_f32_e32 v38, 0xbfb8aa3b, v38
	v_add_f32_e32 v28, 1.0, v28
	v_exp_f32_e32 v40, v38
	v_rcp_f32_e32 v42, v28
	v_add_f32_e32 v28, 1.0, v29
	v_med3_f32 v38, v39, s35, v177
	v_med3_f32 v29, v30, s35, v177
	v_mul_f32_e32 v38, 0xbfb8aa3b, v38
	v_mul_f32_e32 v29, 0xbfb8aa3b, v29
	v_med3_f32 v30, v31, s35, v177
	v_exp_f32_e32 v41, v38
	v_cvt_pk_f32_fp8_sdwa v[38:39], v157 src0_sel:WORD_1
	v_exp_f32_e32 v29, v29
	v_mul_f32_e32 v30, 0xbfb8aa3b, v30
	v_exp_f32_e32 v31, v30
	v_rcp_f32_e32 v43, v28
	v_add_f32_e32 v28, 1.0, v29
	v_rcp_f32_e32 v30, v28
	v_add_f32_e32 v28, 1.0, v31
	v_med3_f32 v29, v38, s35, v177
	v_mul_f32_e32 v29, 0xbfb8aa3b, v29
	v_med3_f32 v31, v39, s35, v177
	v_exp_f32_e32 v29, v29
	v_mul_f32_e32 v31, 0xbfb8aa3b, v31
	v_exp_f32_e32 v39, v31
	v_rcp_f32_e32 v31, v28
	v_add_f32_e32 v28, 1.0, v29
	v_add_f32_e32 v40, 1.0, v40
	v_add_f32_e32 v41, 1.0, v41
	v_rcp_f32_e32 v38, v28
	v_add_f32_e32 v28, 1.0, v39
	v_rcp_f32_e32 v40, v40
	v_rcp_f32_e32 v41, v41
	v_rcp_f32_e32 v39, v28
	v_pk_mul_f32 v[30:31], v[90:91], v[30:31]
	v_pk_mul_f32 v[28:29], v[82:83], v[40:41]
	v_pk_mul_f32 v[40:41], v[84:85], v[42:43]
	v_pk_mul_f32 v[38:39], v[92:93], v[38:39]
	v_cvt_pk_bf16_f32 v28, v28, v29
	v_cvt_pk_bf16_f32 v29, v40, v41
	v_cvt_pk_bf16_f32 v30, v30, v31
	v_cvt_pk_bf16_f32 v31, v38, v39
	global_store_dwordx4 v[32:33], v[28:31], off offset:256
	s_waitcnt vmcnt(15)
	v_cvt_pk_f32_fp8_e32 v[38:39], v154
	v_cvt_pk_f32_fp8_sdwa v[28:29], v154 src0_sel:WORD_1
	v_cvt_pk_f32_fp8_e32 v[30:31], v155
	v_med3_f32 v32, v38, s35, v177
	v_mul_f32_e32 v32, 0xbfb8aa3b, v32
	v_med3_f32 v28, v28, s35, v177
	v_mul_f32_e32 v28, 0xbfb8aa3b, v28
	v_med3_f32 v29, v29, s35, v177
	v_exp_f32_e32 v28, v28
	v_mul_f32_e32 v29, 0xbfb8aa3b, v29
	v_exp_f32_e32 v29, v29
	v_exp_f32_e32 v38, v32
	v_add_f32_e32 v28, 1.0, v28
	v_rcp_f32_e32 v40, v28
	v_add_f32_e32 v28, 1.0, v29
	v_med3_f32 v32, v39, s35, v177
	v_med3_f32 v29, v30, s35, v177
	v_mul_f32_e32 v32, 0xbfb8aa3b, v32
	v_mul_f32_e32 v29, 0xbfb8aa3b, v29
	v_med3_f32 v30, v31, s35, v177
	v_exp_f32_e32 v39, v32
	v_cvt_pk_f32_fp8_sdwa v[32:33], v155 src0_sel:WORD_1
	v_exp_f32_e32 v29, v29
	v_mul_f32_e32 v30, 0xbfb8aa3b, v30
	v_exp_f32_e32 v31, v30
	v_rcp_f32_e32 v41, v28
	v_add_f32_e32 v28, 1.0, v29
	v_rcp_f32_e32 v30, v28
	v_add_f32_e32 v28, 1.0, v31
	v_med3_f32 v29, v32, s35, v177
	v_mul_f32_e32 v29, 0xbfb8aa3b, v29
	v_med3_f32 v31, v33, s35, v177
	v_exp_f32_e32 v29, v29
	v_mul_f32_e32 v31, 0xbfb8aa3b, v31
	v_exp_f32_e32 v33, v31
	v_rcp_f32_e32 v31, v28
	v_add_f32_e32 v28, 1.0, v29
	v_rcp_f32_e32 v32, v28
	v_add_f32_e32 v28, 1.0, v33
	v_add_f32_e32 v38, 1.0, v38
	v_add_f32_e32 v39, 1.0, v39
	v_rcp_f32_e32 v33, v28
	v_rcp_f32_e32 v38, v38
	v_rcp_f32_e32 v39, v39
	v_pk_mul_f32 v[30:31], v[102:103], v[30:31]
	v_pk_mul_f32 v[32:33], v[104:105], v[32:33]
	v_cvt_pk_bf16_f32 v30, v30, v31
	v_pk_mul_f32 v[28:29], v[94:95], v[38:39]
	v_pk_mul_f32 v[38:39], v[96:97], v[40:41]
	v_cvt_pk_bf16_f32 v31, v32, v33
	v_add_co_u32_e32 v32, vcc, s2, v26
	v_cvt_pk_bf16_f32 v28, v28, v29
	v_cvt_pk_bf16_f32 v29, v38, v39
	v_addc_co_u32_e32 v33, vcc, 0, v27, vcc
	global_store_dwordx4 v[32:33], v[28:31], off
	s_waitcnt vmcnt(15)
	v_cvt_pk_f32_fp8_e32 v[38:39], v152
	s_mov_b32 s2, 0x40000
	v_cvt_pk_f32_fp8_sdwa v[28:29], v152 src0_sel:WORD_1
	v_cvt_pk_f32_fp8_e32 v[30:31], v153
	v_med3_f32 v38, v38, s35, v177
	v_med3_f32 v28, v28, s35, v177
	v_mul_f32_e32 v28, 0xbfb8aa3b, v28
	v_med3_f32 v29, v29, s35, v177
	v_exp_f32_e32 v28, v28
	v_mul_f32_e32 v29, 0xbfb8aa3b, v29
	v_exp_f32_e32 v29, v29
	v_mul_f32_e32 v38, 0xbfb8aa3b, v38
	v_add_f32_e32 v28, 1.0, v28
	v_exp_f32_e32 v40, v38
	v_rcp_f32_e32 v42, v28
	v_add_f32_e32 v28, 1.0, v29
	v_med3_f32 v38, v39, s35, v177
	v_med3_f32 v29, v30, s35, v177
	v_mul_f32_e32 v38, 0xbfb8aa3b, v38
	v_mul_f32_e32 v29, 0xbfb8aa3b, v29
	v_med3_f32 v30, v31, s35, v177
	v_exp_f32_e32 v41, v38
	v_cvt_pk_f32_fp8_sdwa v[38:39], v153 src0_sel:WORD_1
	v_exp_f32_e32 v29, v29
	v_mul_f32_e32 v30, 0xbfb8aa3b, v30
	v_exp_f32_e32 v31, v30
	v_rcp_f32_e32 v43, v28
	v_add_f32_e32 v28, 1.0, v29
	v_rcp_f32_e32 v30, v28
	v_add_f32_e32 v28, 1.0, v31
	v_med3_f32 v29, v38, s35, v177
	v_mul_f32_e32 v29, 0xbfb8aa3b, v29
	v_med3_f32 v31, v39, s35, v177
	v_exp_f32_e32 v29, v29
	v_mul_f32_e32 v31, 0xbfb8aa3b, v31
	v_exp_f32_e32 v39, v31
	v_rcp_f32_e32 v31, v28
	v_add_f32_e32 v28, 1.0, v29
	v_add_f32_e32 v40, 1.0, v40
	v_add_f32_e32 v41, 1.0, v41
	v_rcp_f32_e32 v38, v28
	v_add_f32_e32 v28, 1.0, v39
	v_rcp_f32_e32 v40, v40
	v_rcp_f32_e32 v41, v41
	v_rcp_f32_e32 v39, v28
	v_pk_mul_f32 v[30:31], v[114:115], v[30:31]
	v_pk_mul_f32 v[28:29], v[106:107], v[40:41]
	v_pk_mul_f32 v[40:41], v[108:109], v[42:43]
	v_pk_mul_f32 v[38:39], v[116:117], v[38:39]
	v_cvt_pk_bf16_f32 v28, v28, v29
	v_cvt_pk_bf16_f32 v29, v40, v41
	v_cvt_pk_bf16_f32 v30, v30, v31
	v_cvt_pk_bf16_f32 v31, v38, v39
	global_store_dwordx4 v[32:33], v[28:31], off offset:256
	s_waitcnt vmcnt(15)
	v_cvt_pk_f32_fp8_e32 v[38:39], v150
	v_cvt_pk_f32_fp8_sdwa v[28:29], v150 src0_sel:WORD_1
	v_cvt_pk_f32_fp8_e32 v[30:31], v151
	v_med3_f32 v32, v38, s35, v177
	v_mul_f32_e32 v32, 0xbfb8aa3b, v32
	v_med3_f32 v28, v28, s35, v177
	v_mul_f32_e32 v28, 0xbfb8aa3b, v28
	v_med3_f32 v29, v29, s35, v177
	v_exp_f32_e32 v28, v28
	v_mul_f32_e32 v29, 0xbfb8aa3b, v29
	v_exp_f32_e32 v29, v29
	v_exp_f32_e32 v38, v32
	v_add_f32_e32 v28, 1.0, v28
	v_rcp_f32_e32 v40, v28
	v_add_f32_e32 v28, 1.0, v29
	v_med3_f32 v32, v39, s35, v177
	v_med3_f32 v29, v30, s35, v177
	v_mul_f32_e32 v32, 0xbfb8aa3b, v32
	v_mul_f32_e32 v29, 0xbfb8aa3b, v29
	v_med3_f32 v30, v31, s35, v177
	v_exp_f32_e32 v39, v32
	v_cvt_pk_f32_fp8_sdwa v[32:33], v151 src0_sel:WORD_1
	v_exp_f32_e32 v29, v29
	v_mul_f32_e32 v30, 0xbfb8aa3b, v30
	v_exp_f32_e32 v31, v30
	v_rcp_f32_e32 v41, v28
	v_add_f32_e32 v28, 1.0, v29
	v_rcp_f32_e32 v30, v28
	v_add_f32_e32 v28, 1.0, v31
	v_med3_f32 v29, v32, s35, v177
	v_mul_f32_e32 v29, 0xbfb8aa3b, v29
	v_med3_f32 v31, v33, s35, v177
	v_exp_f32_e32 v29, v29
	v_mul_f32_e32 v31, 0xbfb8aa3b, v31
	v_exp_f32_e32 v33, v31
	v_rcp_f32_e32 v31, v28
	v_add_f32_e32 v28, 1.0, v29
	v_rcp_f32_e32 v32, v28
	v_add_f32_e32 v28, 1.0, v33
	v_add_f32_e32 v38, 1.0, v38
	v_add_f32_e32 v39, 1.0, v39
	v_rcp_f32_e32 v33, v28
	v_rcp_f32_e32 v38, v38
	v_rcp_f32_e32 v39, v39
	v_pk_mul_f32 v[30:31], v[126:127], v[30:31]
	v_pk_mul_f32 v[32:33], v[128:129], v[32:33]
	v_cvt_pk_bf16_f32 v30, v30, v31
	v_pk_mul_f32 v[28:29], v[118:119], v[38:39]
	v_pk_mul_f32 v[38:39], v[120:121], v[40:41]
	v_cvt_pk_bf16_f32 v31, v32, v33
	v_add_co_u32_e32 v32, vcc, s2, v26
	v_cvt_pk_bf16_f32 v28, v28, v29
	v_cvt_pk_bf16_f32 v29, v38, v39
	v_addc_co_u32_e32 v33, vcc, 0, v27, vcc
	global_store_dwordx4 v[32:33], v[28:31], off
	s_waitcnt vmcnt(15)
	v_cvt_pk_f32_fp8_e32 v[38:39], v148
	s_mov_b32 s2, 0x48000
	v_cvt_pk_f32_fp8_sdwa v[28:29], v148 src0_sel:WORD_1
	v_cvt_pk_f32_fp8_e32 v[30:31], v149
	v_med3_f32 v38, v38, s35, v177
	v_med3_f32 v28, v28, s35, v177
	v_mul_f32_e32 v28, 0xbfb8aa3b, v28
	v_med3_f32 v29, v29, s35, v177
	v_exp_f32_e32 v28, v28
	v_mul_f32_e32 v29, 0xbfb8aa3b, v29
	v_exp_f32_e32 v29, v29
	v_mul_f32_e32 v38, 0xbfb8aa3b, v38
	v_add_f32_e32 v28, 1.0, v28
	v_exp_f32_e32 v40, v38
	v_rcp_f32_e32 v42, v28
	v_add_f32_e32 v28, 1.0, v29
	v_med3_f32 v38, v39, s35, v177
	v_med3_f32 v29, v30, s35, v177
	v_mul_f32_e32 v38, 0xbfb8aa3b, v38
	v_mul_f32_e32 v29, 0xbfb8aa3b, v29
	v_med3_f32 v30, v31, s35, v177
	v_exp_f32_e32 v41, v38
	v_cvt_pk_f32_fp8_sdwa v[38:39], v149 src0_sel:WORD_1
	v_exp_f32_e32 v29, v29
	v_mul_f32_e32 v30, 0xbfb8aa3b, v30
	v_exp_f32_e32 v31, v30
	v_rcp_f32_e32 v43, v28
	v_add_f32_e32 v28, 1.0, v29
	v_rcp_f32_e32 v30, v28
	v_add_f32_e32 v28, 1.0, v31
	v_med3_f32 v29, v38, s35, v177
	v_mul_f32_e32 v29, 0xbfb8aa3b, v29
	v_med3_f32 v31, v39, s35, v177
	v_exp_f32_e32 v29, v29
	v_mul_f32_e32 v31, 0xbfb8aa3b, v31
	v_exp_f32_e32 v39, v31
	v_rcp_f32_e32 v31, v28
	v_add_f32_e32 v28, 1.0, v29
	v_add_f32_e32 v40, 1.0, v40
	v_add_f32_e32 v41, 1.0, v41
	v_rcp_f32_e32 v38, v28
	v_add_f32_e32 v28, 1.0, v39
	v_rcp_f32_e32 v40, v40
	v_rcp_f32_e32 v41, v41
	v_rcp_f32_e32 v39, v28
	v_pk_mul_f32 v[30:31], v[110:111], v[30:31]
	v_pk_mul_f32 v[28:29], v[122:123], v[40:41]
	v_pk_mul_f32 v[40:41], v[124:125], v[42:43]
	v_pk_mul_f32 v[38:39], v[112:113], v[38:39]
	v_cvt_pk_bf16_f32 v28, v28, v29
	v_cvt_pk_bf16_f32 v29, v40, v41
	v_cvt_pk_bf16_f32 v30, v30, v31
	v_cvt_pk_bf16_f32 v31, v38, v39
	global_store_dwordx4 v[32:33], v[28:31], off offset:256
	s_waitcnt vmcnt(15)
	v_cvt_pk_f32_fp8_e32 v[38:39], v146
	v_cvt_pk_f32_fp8_sdwa v[28:29], v146 src0_sel:WORD_1
	v_cvt_pk_f32_fp8_e32 v[30:31], v147
	v_med3_f32 v32, v38, s35, v177
	v_mul_f32_e32 v32, 0xbfb8aa3b, v32
	v_med3_f32 v28, v28, s35, v177
	v_mul_f32_e32 v28, 0xbfb8aa3b, v28
	v_med3_f32 v29, v29, s35, v177
	v_exp_f32_e32 v28, v28
	v_mul_f32_e32 v29, 0xbfb8aa3b, v29
	v_exp_f32_e32 v29, v29
	v_exp_f32_e32 v38, v32
	v_add_f32_e32 v28, 1.0, v28
	v_rcp_f32_e32 v40, v28
	v_add_f32_e32 v28, 1.0, v29
	v_med3_f32 v32, v39, s35, v177
	v_med3_f32 v29, v30, s35, v177
	v_mul_f32_e32 v32, 0xbfb8aa3b, v32
	v_mul_f32_e32 v29, 0xbfb8aa3b, v29
	v_med3_f32 v30, v31, s35, v177
	v_exp_f32_e32 v39, v32
	v_cvt_pk_f32_fp8_sdwa v[32:33], v147 src0_sel:WORD_1
	v_exp_f32_e32 v29, v29
	v_mul_f32_e32 v30, 0xbfb8aa3b, v30
	v_exp_f32_e32 v31, v30
	v_rcp_f32_e32 v41, v28
	v_add_f32_e32 v28, 1.0, v29
	v_rcp_f32_e32 v30, v28
	v_add_f32_e32 v28, 1.0, v31
	v_med3_f32 v29, v32, s35, v177
	v_mul_f32_e32 v29, 0xbfb8aa3b, v29
	v_med3_f32 v31, v33, s35, v177
	v_exp_f32_e32 v29, v29
	v_mul_f32_e32 v31, 0xbfb8aa3b, v31
	v_exp_f32_e32 v33, v31
	v_rcp_f32_e32 v31, v28
	v_add_f32_e32 v28, 1.0, v29
	v_rcp_f32_e32 v32, v28
	v_add_f32_e32 v28, 1.0, v33
	v_add_f32_e32 v38, 1.0, v38
	v_add_f32_e32 v39, 1.0, v39
	v_rcp_f32_e32 v33, v28
	v_rcp_f32_e32 v38, v38
	v_rcp_f32_e32 v39, v39
	v_pk_mul_f32 v[30:31], v[86:87], v[30:31]
	v_pk_mul_f32 v[32:33], v[88:89], v[32:33]
	v_cvt_pk_bf16_f32 v30, v30, v31
	v_pk_mul_f32 v[28:29], v[98:99], v[38:39]
	v_pk_mul_f32 v[38:39], v[100:101], v[40:41]
	v_cvt_pk_bf16_f32 v31, v32, v33
	v_add_co_u32_e32 v32, vcc, s2, v26
	v_cvt_pk_bf16_f32 v28, v28, v29
	v_cvt_pk_bf16_f32 v29, v38, v39
	v_addc_co_u32_e32 v33, vcc, 0, v27, vcc
	global_store_dwordx4 v[32:33], v[28:31], off
	s_waitcnt vmcnt(15)
	v_cvt_pk_f32_fp8_e32 v[38:39], v144
	s_mov_b32 s2, 0x50000
	v_cvt_pk_f32_fp8_sdwa v[28:29], v144 src0_sel:WORD_1
	v_cvt_pk_f32_fp8_e32 v[30:31], v145
	v_med3_f32 v38, v38, s35, v177
	v_med3_f32 v28, v28, s35, v177
	v_mul_f32_e32 v28, 0xbfb8aa3b, v28
	v_med3_f32 v29, v29, s35, v177
	v_exp_f32_e32 v28, v28
	v_mul_f32_e32 v29, 0xbfb8aa3b, v29
	v_exp_f32_e32 v29, v29
	v_mul_f32_e32 v38, 0xbfb8aa3b, v38
	v_add_f32_e32 v28, 1.0, v28
	v_exp_f32_e32 v40, v38
	v_rcp_f32_e32 v42, v28
	v_add_f32_e32 v28, 1.0, v29
	v_med3_f32 v38, v39, s35, v177
	v_med3_f32 v29, v30, s35, v177
	v_mul_f32_e32 v38, 0xbfb8aa3b, v38
	v_mul_f32_e32 v29, 0xbfb8aa3b, v29
	v_med3_f32 v30, v31, s35, v177
	v_exp_f32_e32 v41, v38
	v_cvt_pk_f32_fp8_sdwa v[38:39], v145 src0_sel:WORD_1
	v_exp_f32_e32 v29, v29
	v_mul_f32_e32 v30, 0xbfb8aa3b, v30
	v_exp_f32_e32 v31, v30
	v_rcp_f32_e32 v43, v28
	v_add_f32_e32 v28, 1.0, v29
	v_rcp_f32_e32 v30, v28
	v_add_f32_e32 v28, 1.0, v31
	v_med3_f32 v29, v38, s35, v177
	v_mul_f32_e32 v29, 0xbfb8aa3b, v29
	v_med3_f32 v31, v39, s35, v177
	v_exp_f32_e32 v29, v29
	v_mul_f32_e32 v31, 0xbfb8aa3b, v31
	v_exp_f32_e32 v39, v31
	v_rcp_f32_e32 v31, v28
	v_add_f32_e32 v28, 1.0, v29
	v_add_f32_e32 v40, 1.0, v40
	v_add_f32_e32 v41, 1.0, v41
	v_rcp_f32_e32 v38, v28
	v_add_f32_e32 v28, 1.0, v39
	v_rcp_f32_e32 v40, v40
	v_rcp_f32_e32 v41, v41
	v_rcp_f32_e32 v39, v28
	v_pk_mul_f32 v[30:31], v[58:59], v[30:31]
	v_pk_mul_f32 v[28:29], v[70:71], v[40:41]
	v_pk_mul_f32 v[40:41], v[72:73], v[42:43]
	v_pk_mul_f32 v[38:39], v[60:61], v[38:39]
	v_cvt_pk_bf16_f32 v28, v28, v29
	v_cvt_pk_bf16_f32 v29, v40, v41
	v_cvt_pk_bf16_f32 v30, v30, v31
	v_cvt_pk_bf16_f32 v31, v38, v39
	global_store_dwordx4 v[32:33], v[28:31], off offset:256
	s_waitcnt vmcnt(15)
	v_cvt_pk_f32_fp8_e32 v[38:39], v142
	v_cvt_pk_f32_fp8_sdwa v[28:29], v142 src0_sel:WORD_1
	v_cvt_pk_f32_fp8_e32 v[30:31], v143
	v_med3_f32 v32, v38, s35, v177
	v_mul_f32_e32 v32, 0xbfb8aa3b, v32
	v_med3_f32 v28, v28, s35, v177
	v_mul_f32_e32 v28, 0xbfb8aa3b, v28
	v_med3_f32 v29, v29, s35, v177
	v_exp_f32_e32 v28, v28
	v_mul_f32_e32 v29, 0xbfb8aa3b, v29
	v_exp_f32_e32 v29, v29
	v_exp_f32_e32 v38, v32
	v_add_f32_e32 v28, 1.0, v28
	v_rcp_f32_e32 v40, v28
	v_add_f32_e32 v28, 1.0, v29
	v_med3_f32 v29, v30, s35, v177
	v_med3_f32 v32, v39, s35, v177
	v_mul_f32_e32 v29, 0xbfb8aa3b, v29
	v_med3_f32 v30, v31, s35, v177
	v_mul_f32_e32 v32, 0xbfb8aa3b, v32
	v_exp_f32_e32 v29, v29
	v_mul_f32_e32 v30, 0xbfb8aa3b, v30
	v_exp_f32_e32 v39, v32
	v_cvt_pk_f32_fp8_sdwa v[32:33], v143 src0_sel:WORD_1
	v_exp_f32_e32 v31, v30
	v_rcp_f32_e32 v41, v28
	v_add_f32_e32 v28, 1.0, v29
	v_rcp_f32_e32 v30, v28
	v_add_f32_e32 v28, 1.0, v31
	v_med3_f32 v29, v32, s35, v177
	v_med3_f32 v31, v33, s35, v177
	v_mul_f32_e32 v29, 0xbfb8aa3b, v29
	v_mul_f32_e32 v31, 0xbfb8aa3b, v31
	v_exp_f32_e32 v29, v29
	v_exp_f32_e32 v33, v31
	v_rcp_f32_e32 v31, v28
	v_add_f32_e32 v38, 1.0, v38
	v_add_f32_e32 v28, 1.0, v29
	v_rcp_f32_e32 v32, v28
	v_pk_mul_f32 v[30:31], v[34:35], v[30:31]
	s_waitcnt vmcnt(14)
	v_cvt_pk_f32_fp8_e32 v[34:35], v140
	v_add_f32_e32 v28, 1.0, v33
	v_add_f32_e32 v39, 1.0, v39
	v_rcp_f32_e32 v33, v28
	v_rcp_f32_e32 v38, v38
	v_rcp_f32_e32 v39, v39
	v_med3_f32 v34, v34, s35, v177
	v_pk_mul_f32 v[32:33], v[36:37], v[32:33]
	v_mul_f32_e32 v34, 0xbfb8aa3b, v34
	v_pk_mul_f32 v[28:29], v[46:47], v[38:39]
	v_pk_mul_f32 v[38:39], v[48:49], v[40:41]
	v_cvt_pk_bf16_f32 v30, v30, v31
	v_cvt_pk_bf16_f32 v31, v32, v33
	v_add_co_u32_e32 v32, vcc, s2, v26
	v_exp_f32_e32 v36, v34
	v_cvt_pk_bf16_f32 v28, v28, v29
	v_cvt_pk_bf16_f32 v29, v38, v39
	v_addc_co_u32_e32 v33, vcc, 0, v27, vcc
	v_med3_f32 v34, v35, s35, v177
	global_store_dwordx4 v[32:33], v[28:31], off
	v_mul_f32_e32 v34, 0xbfb8aa3b, v34
	v_exp_f32_e32 v37, v34
	v_cvt_pk_f32_fp8_sdwa v[28:29], v140 src0_sel:WORD_1
	v_cvt_pk_f32_fp8_e32 v[30:31], v141
	v_cvt_pk_f32_fp8_sdwa v[34:35], v141 src0_sel:WORD_1
	v_add_f32_e32 v36, 1.0, v36
	v_med3_f32 v28, v28, s35, v177
	v_med3_f32 v29, v29, s35, v177
	v_med3_f32 v30, v30, s35, v177
	v_med3_f32 v31, v31, s35, v177
	v_mul_f32_e32 v28, 0xbfb8aa3b, v28
	v_mul_f32_e32 v29, 0xbfb8aa3b, v29
	v_mul_f32_e32 v30, 0xbfb8aa3b, v30
	v_mul_f32_e32 v31, 0xbfb8aa3b, v31
	v_med3_f32 v34, v34, s35, v177
	v_med3_f32 v35, v35, s35, v177
	v_exp_f32_e32 v28, v28
	v_exp_f32_e32 v29, v29
	v_exp_f32_e32 v30, v30
	v_exp_f32_e32 v31, v31
	v_mul_f32_e32 v34, 0xbfb8aa3b, v34
	v_mul_f32_e32 v35, 0xbfb8aa3b, v35
	v_exp_f32_e32 v34, v34
	v_exp_f32_e32 v35, v35
	v_add_f32_e32 v37, 1.0, v37
	v_add_f32_e32 v28, 1.0, v28
	v_add_f32_e32 v29, 1.0, v29
	v_add_f32_e32 v30, 1.0, v30
	v_add_f32_e32 v31, 1.0, v31
	v_rcp_f32_e32 v36, v36
	v_rcp_f32_e32 v37, v37
	v_rcp_f32_e32 v28, v28
	v_rcp_f32_e32 v29, v29
	v_rcp_f32_e32 v30, v30
	v_rcp_f32_e32 v31, v31
	v_add_f32_e32 v34, 1.0, v34
	v_add_f32_e32 v35, 1.0, v35
	v_rcp_f32_e32 v34, v34
	v_rcp_f32_e32 v35, v35
	v_pk_mul_f32 v[22:23], v[22:23], v[36:37]
	v_pk_mul_f32 v[24:25], v[24:25], v[28:29]
	v_pk_mul_f32 v[18:19], v[18:19], v[30:31]
	v_cvt_pk_bf16_f32 v22, v22, v23
	v_cvt_pk_bf16_f32 v23, v24, v25
	v_cvt_pk_bf16_f32 v24, v18, v19
	v_pk_mul_f32 v[18:19], v[20:21], v[34:35]
	s_waitcnt vmcnt(14)
	v_cvt_pk_f32_fp8_sdwa v[20:21], v138 src0_sel:WORD_1
	v_cvt_pk_bf16_f32 v25, v18, v19
	v_cvt_pk_f32_fp8_e32 v[18:19], v138
	global_store_dwordx4 v[32:33], v[22:25], off offset:256
	v_med3_f32 v18, v18, s35, v177
	v_mul_f32_e32 v18, 0xbfb8aa3b, v18
	v_exp_f32_e32 v24, v18
	v_med3_f32 v18, v19, s35, v177
	v_cvt_pk_f32_fp8_e32 v[22:23], v139
	v_mul_f32_e32 v18, 0xbfb8aa3b, v18
	v_exp_f32_e32 v25, v18
	v_cvt_pk_f32_fp8_sdwa v[18:19], v139 src0_sel:WORD_1
	v_med3_f32 v20, v20, s35, v177
	v_med3_f32 v21, v21, s35, v177
	v_med3_f32 v22, v22, s35, v177
	v_med3_f32 v23, v23, s35, v177
	v_mul_f32_e32 v20, 0xbfb8aa3b, v20
	v_mul_f32_e32 v21, 0xbfb8aa3b, v21
	v_mul_f32_e32 v22, 0xbfb8aa3b, v22
	v_mul_f32_e32 v23, 0xbfb8aa3b, v23
	v_med3_f32 v18, v18, s35, v177
	v_med3_f32 v19, v19, s35, v177
	v_exp_f32_e32 v20, v20
	v_exp_f32_e32 v21, v21
	v_exp_f32_e32 v22, v22
	v_exp_f32_e32 v23, v23
	v_mul_f32_e32 v18, 0xbfb8aa3b, v18
	v_mul_f32_e32 v19, 0xbfb8aa3b, v19
	v_exp_f32_e32 v18, v18
	v_exp_f32_e32 v19, v19
	v_add_f32_e32 v24, 1.0, v24
	v_add_f32_e32 v25, 1.0, v25
	v_add_f32_e32 v20, 1.0, v20
	v_add_f32_e32 v21, 1.0, v21
	v_add_f32_e32 v22, 1.0, v22
	v_add_f32_e32 v23, 1.0, v23
	v_rcp_f32_e32 v24, v24
	v_rcp_f32_e32 v25, v25
	v_rcp_f32_e32 v20, v20
	v_rcp_f32_e32 v21, v21
	v_rcp_f32_e32 v22, v22
	v_rcp_f32_e32 v23, v23
	v_add_f32_e32 v18, 1.0, v18
	v_add_f32_e32 v19, 1.0, v19
	v_rcp_f32_e32 v18, v18
	v_rcp_f32_e32 v19, v19
	v_pk_mul_f32 v[14:15], v[14:15], v[24:25]
	v_pk_mul_f32 v[16:17], v[16:17], v[20:21]
	v_pk_mul_f32 v[10:11], v[10:11], v[22:23]
	v_cvt_pk_bf16_f32 v14, v14, v15
	v_cvt_pk_bf16_f32 v15, v16, v17
	v_cvt_pk_bf16_f32 v16, v10, v11
	v_pk_mul_f32 v[10:11], v[12:13], v[18:19]
	s_waitcnt vmcnt(14)
	v_cvt_pk_f32_fp8_e32 v[12:13], v136
	s_mov_b32 s2, 0x58000
	v_cvt_pk_bf16_f32 v17, v10, v11
	v_add_co_u32_e32 v10, vcc, s2, v26
	v_med3_f32 v12, v12, s35, v177
	v_mul_f32_e32 v12, 0xbfb8aa3b, v12
	v_exp_f32_e32 v18, v12
	v_addc_co_u32_e32 v11, vcc, 0, v27, vcc
	v_med3_f32 v12, v13, s35, v177
	global_store_dwordx4 v[10:11], v[14:17], off
	v_mul_f32_e32 v12, 0xbfb8aa3b, v12
	v_exp_f32_e32 v19, v12
	v_cvt_pk_f32_fp8_sdwa v[14:15], v136 src0_sel:WORD_1
	v_cvt_pk_f32_fp8_e32 v[16:17], v137
	v_cvt_pk_f32_fp8_sdwa v[12:13], v137 src0_sel:WORD_1
	v_add_f32_e32 v18, 1.0, v18
	v_med3_f32 v14, v14, s35, v177
	v_med3_f32 v15, v15, s35, v177
	v_med3_f32 v16, v16, s35, v177
	v_med3_f32 v17, v17, s35, v177
	v_mul_f32_e32 v14, 0xbfb8aa3b, v14
	v_mul_f32_e32 v15, 0xbfb8aa3b, v15
	v_mul_f32_e32 v16, 0xbfb8aa3b, v16
	v_mul_f32_e32 v17, 0xbfb8aa3b, v17
	v_med3_f32 v12, v12, s35, v177
	v_med3_f32 v13, v13, s35, v177
	v_exp_f32_e32 v14, v14
	v_exp_f32_e32 v15, v15
	v_exp_f32_e32 v16, v16
	v_exp_f32_e32 v17, v17
	v_mul_f32_e32 v12, 0xbfb8aa3b, v12
	v_mul_f32_e32 v13, 0xbfb8aa3b, v13
	v_exp_f32_e32 v12, v12
	v_exp_f32_e32 v13, v13
	v_add_f32_e32 v19, 1.0, v19
	v_add_f32_e32 v14, 1.0, v14
	v_add_f32_e32 v15, 1.0, v15
	v_add_f32_e32 v16, 1.0, v16
	v_add_f32_e32 v17, 1.0, v17
	v_rcp_f32_e32 v18, v18
	v_rcp_f32_e32 v19, v19
	v_rcp_f32_e32 v14, v14
	v_rcp_f32_e32 v15, v15
	v_rcp_f32_e32 v16, v16
	v_rcp_f32_e32 v17, v17
	v_add_f32_e32 v12, 1.0, v12
	v_add_f32_e32 v13, 1.0, v13
	v_rcp_f32_e32 v12, v12
	v_rcp_f32_e32 v13, v13
	v_pk_mul_f32 v[6:7], v[6:7], v[18:19]
	v_pk_mul_f32 v[8:9], v[8:9], v[14:15]
	v_pk_mul_f32 v[2:3], v[2:3], v[16:17]
	v_cvt_pk_bf16_f32 v6, v6, v7
	v_cvt_pk_bf16_f32 v7, v8, v9
	v_cvt_pk_bf16_f32 v8, v2, v3
	v_pk_mul_f32 v[2:3], v[4:5], v[12:13]
	s_andn2_b64 vcc, exec, s[4:5]
	v_cvt_pk_bf16_f32 v9, v2, v3
	s_mov_b64 s[4:5], -1
	global_store_dwordx4 v[10:11], v[6:9], off offset:256
	s_cbranch_vccnz .LBB0_1038
	s_andn2_b64 vcc, exec, s[12:13]
	s_cbranch_vccnz .LBB0_1037
	s_barrier
	s_branch .LBB0_1037
